# RG final pass output gating: the eight gr loads of a unit issued up front (were serialised load -> vmcnt(0) -> compute -> store by the in-place aliasing), rounds wait vmcnt(7)
# baseline (speedup 1.0000x reference)
.LBB0_621:
	v_add_u32_e32 v128, 0, v117
	v_add_u32_e32 v34, 0x1c200, v128
	v_add_u32_e32 v35, 0x1c300, v128
	v_add_u32_e32 v36, 0x1c400, v128
	v_add_u32_e32 v37, 0x1c500, v128
	v_add_u32_e32 v38, 0x1c600, v128
	v_add_u32_e32 v118, 0, v0
	ds_read_b32 v34, v34
	ds_read_b32 v35, v35
	ds_read_b32 v36, v36
	ds_read_b32 v37, v37
	ds_read_b32 v127, v38
	ds_read_u16 v38, v118
	ds_read_u16 v40, v118 offset:288
	ds_read_u16 v42, v118 offset:576
	ds_read_u16 v44, v118 offset:864
	ds_read_u16 v39, v118 offset:144
	ds_read_u16 v41, v118 offset:432
	ds_read_u16 v43, v118 offset:720
	v_add_u32_e32 v68, 0x1c700, v128
	ds_read_b32 v143, v68
	s_waitcnt lgkmcnt(7)
	v_lshlrev_b32_e32 v38, 16, v38
	v_add_u32_e32 v68, 0x1c900, v128
	v_fma_f32 v119, v34, v38, v127
	ds_read_u16 v38, v118 offset:2304
	ds_read_b32 v137, v68
	s_waitcnt lgkmcnt(5)
	v_lshlrev_b32_e32 v39, 16, v39
	v_lshlrev_b32_e32 v40, 16, v40
	v_fmac_f32_e32 v119, v35, v39
	v_fma_f32 v120, v34, v39, v127
	ds_read_u16 v39, v118 offset:2448
	s_waitcnt lgkmcnt(5)
	v_lshlrev_b32_e32 v41, 16, v41
	v_fmac_f32_e32 v119, v36, v40
	v_fmac_f32_e32 v120, v35, v40
	v_fma_f32 v121, v34, v40, v127
	ds_read_u16 v40, v118 offset:2592
	v_lshlrev_b32_e32 v42, 16, v42
	v_fmac_f32_e32 v119, v37, v41
	v_fmac_f32_e32 v120, v36, v41
	v_fmac_f32_e32 v121, v35, v41
	v_fma_f32 v122, v34, v41, v127
	ds_read_u16 v41, v118 offset:2736
	s_waitcnt lgkmcnt(6)
	v_lshlrev_b32_e32 v43, 16, v43
	v_fmac_f32_e32 v120, v37, v42
	v_fmac_f32_e32 v121, v36, v42
	v_fmac_f32_e32 v122, v35, v42
	ds_read_u16 v42, v118 offset:2880
	v_lshlrev_b32_e32 v44, 16, v44
	v_fmac_f32_e32 v121, v37, v43
	v_fmac_f32_e32 v122, v36, v43
	s_waitcnt lgkmcnt(5)
	v_lshlrev_b32_e32 v38, 16, v38
	ds_read_u16 v43, v118 offset:3024
	v_fmac_f32_e32 v122, v37, v44
	ds_read_u16 v44, v118 offset:3168
	v_fma_f32 v123, v34, v38, v127
	ds_read_u16 v38, v118 offset:4608
	s_waitcnt lgkmcnt(6)
	v_lshlrev_b32_e32 v39, 16, v39
	s_waitcnt lgkmcnt(5)
	v_lshlrev_b32_e32 v40, 16, v40
	v_fmac_f32_e32 v123, v35, v39
	v_fma_f32 v124, v34, v39, v127
	ds_read_u16 v39, v118 offset:4752
	s_waitcnt lgkmcnt(5)
	v_lshlrev_b32_e32 v41, 16, v41
	v_fmac_f32_e32 v123, v36, v40
	v_fmac_f32_e32 v124, v35, v40
	v_fma_f32 v125, v34, v40, v127
	ds_read_u16 v40, v118 offset:4896
	s_waitcnt lgkmcnt(5)
	v_lshlrev_b32_e32 v42, 16, v42
	v_fmac_f32_e32 v123, v37, v41
	v_fmac_f32_e32 v124, v36, v41
	v_fmac_f32_e32 v125, v35, v41
	v_fma_f32 v126, v34, v41, v127
	ds_read_u16 v41, v118 offset:5040
	s_waitcnt lgkmcnt(5)
	v_lshlrev_b32_e32 v43, 16, v43
	v_fmac_f32_e32 v124, v37, v42
	v_fmac_f32_e32 v125, v36, v42
	v_fmac_f32_e32 v126, v35, v42
	ds_read_u16 v42, v118 offset:5184
	s_waitcnt lgkmcnt(5)
	v_lshlrev_b32_e32 v44, 16, v44
	v_fmac_f32_e32 v125, v37, v43
	v_fmac_f32_e32 v126, v36, v43
	s_waitcnt lgkmcnt(4)
	v_lshlrev_b32_e32 v38, 16, v38
	ds_read_u16 v43, v118 offset:5328
	v_fmac_f32_e32 v126, v37, v44
	ds_read_u16 v44, v118 offset:5472
	v_fma_f32 v129, v34, v38, v127
	ds_read_u16 v38, v118 offset:6912
	s_waitcnt lgkmcnt(6)
	v_lshlrev_b32_e32 v39, 16, v39
	s_waitcnt lgkmcnt(5)
	v_lshlrev_b32_e32 v40, 16, v40
	v_fmac_f32_e32 v129, v35, v39
	v_fma_f32 v130, v34, v39, v127
	s_waitcnt lgkmcnt(4)
	v_lshlrev_b32_e32 v41, 16, v41
	v_fmac_f32_e32 v129, v36, v40
	v_fmac_f32_e32 v130, v35, v40
	v_fma_f32 v131, v34, v40, v127
	s_waitcnt lgkmcnt(3)
	v_lshlrev_b32_e32 v42, 16, v42
	v_fmac_f32_e32 v129, v37, v41
	v_fmac_f32_e32 v130, v36, v41
	v_fmac_f32_e32 v131, v35, v41
	v_fma_f32 v132, v34, v41, v127
	ds_read_u16 v39, v118 offset:7056
	ds_read_u16 v40, v118 offset:7200
	ds_read_u16 v41, v118 offset:7344
	s_waitcnt lgkmcnt(5)
	v_lshlrev_b32_e32 v43, 16, v43
	v_fmac_f32_e32 v130, v37, v42
	v_fmac_f32_e32 v131, v36, v42
	v_fmac_f32_e32 v132, v35, v42
	ds_read_u16 v42, v118 offset:7488
	s_waitcnt lgkmcnt(5)
	v_lshlrev_b32_e32 v44, 16, v44
	v_fmac_f32_e32 v131, v37, v43
	v_fmac_f32_e32 v132, v36, v43
	ds_read_u16 v43, v118 offset:7632
	v_fmac_f32_e32 v132, v37, v44
	ds_read_u16 v44, v118 offset:7776
	s_waitcnt lgkmcnt(6)
	v_lshlrev_b32_e32 v38, 16, v38
	s_waitcnt lgkmcnt(5)
	v_lshlrev_b32_e32 v39, 16, v39
	s_waitcnt lgkmcnt(4)
	v_lshlrev_b32_e32 v40, 16, v40
	s_waitcnt lgkmcnt(3)
	v_lshlrev_b32_e32 v41, 16, v41
	s_waitcnt lgkmcnt(2)
	v_lshlrev_b32_e32 v42, 16, v42
	v_fma_f32 v133, v34, v38, v127
	v_fma_f32 v134, v34, v39, v127
	v_fma_f32 v135, v34, v40, v127
	v_fmac_f32_e32 v127, v34, v41
	s_waitcnt lgkmcnt(1)
	v_lshlrev_b32_e32 v43, 16, v43
	v_fmac_f32_e32 v133, v35, v39
	v_fmac_f32_e32 v134, v35, v40
	v_fmac_f32_e32 v135, v35, v41
	v_fmac_f32_e32 v127, v35, v42
	v_add_u32_e32 v136, 0, v116
	s_waitcnt lgkmcnt(0)
	v_lshlrev_b32_e32 v44, 16, v44
	v_fmac_f32_e32 v133, v36, v40
	v_fmac_f32_e32 v134, v36, v41
	v_fmac_f32_e32 v135, v36, v42
	v_fmac_f32_e32 v127, v36, v43
	v_add_u32_e32 v34, 0x13200, v136
	v_fmac_f32_e32 v133, v37, v41
	v_fmac_f32_e32 v134, v37, v42
	v_fmac_f32_e32 v135, v37, v43
	v_fmac_f32_e32 v127, v37, v44
	ds_read_b128 v[34:37], v34
	v_add_u32_e32 v38, 0x13240, v136
	ds_read_b128 v[42:45], v38
	s_waitcnt lgkmcnt(1)
	v_mfma_f32_16x16x32_bf16 v[38:41], v[2:5], v[34:37], 0
	v_add_u32_e32 v50, 0x15640, v136
	ds_read_b128 v[138:141], v50
	v_add_u32_e32 v68, 0x1cb00, v128
	s_waitcnt lgkmcnt(1)
	v_mfma_f32_16x16x32_bf16 v[58:61], v[18:21], v[42:45], v[38:41]
	s_mov_b32 s13, 0x7b300000
	v_mfma_f32_16x16x32_bf16 v[38:41], v[6:9], v[34:37], 0
	v_mfma_f32_16x16x32_bf16 v[46:49], v[22:25], v[42:45], v[38:41]
	s_nop 4
	v_fmamk_f32 v58, v58, 0xbfb8aa3b, v143
	v_exp_f32_e32 v58, v58
	v_fmamk_f32 v59, v59, 0xbfb8aa3b, v143
	v_mfma_f32_16x16x32_bf16 v[38:41], v[10:13], v[34:37], 0
	v_exp_f32_e32 v59, v59
	v_add_f32_e32 v58, 1.0, v58
	v_rcp_f32_e64 v58, -v58
	v_mfma_f32_16x16x32_bf16 v[34:37], v[14:17], v[34:37], 0
	v_add_f32_e32 v59, 1.0, v59
	v_rcp_f32_e64 v59, -v59
	v_fmamk_f32 v60, v60, 0xbfb8aa3b, v143
	v_mfma_f32_16x16x32_bf16 v[38:41], v[26:29], v[42:45], v[38:41]
	v_exp_f32_e32 v60, v60
	v_fmamk_f32 v61, v61, 0xbfb8aa3b, v143
	v_exp_f32_e32 v61, v61
	v_mfma_f32_16x16x32_bf16 v[34:37], v[30:33], v[42:45], v[34:37]
	v_add_u32_e32 v42, 0x15600, v136
	ds_read_b128 v[42:45], v42
	v_add_f32_e32 v60, 1.0, v60
	s_waitcnt lgkmcnt(0)
	v_mfma_f32_16x16x32_bf16 v[50:53], v[2:5], v[42:45], 0
	v_rcp_f32_e64 v60, -v60
	v_add_f32_e32 v61, 1.0, v61
	v_rcp_f32_e64 v61, -v61
	v_mfma_f32_16x16x32_bf16 v[62:65], v[18:21], v[138:141], v[50:53]
	v_mfma_f32_16x16x32_bf16 v[50:53], v[6:9], v[42:45], 0
	v_mfma_f32_16x16x32_bf16 v[54:57], v[22:25], v[138:141], v[50:53]
	s_nop 5
	v_fmamk_f32 v62, v62, 0xbfb8aa3b, v137
	v_exp_f32_e32 v62, v62
	v_mfma_f32_16x16x32_bf16 v[50:53], v[10:13], v[42:45], 0
	v_add_f32_e32 v62, 1.0, v62
	v_rcp_f32_e32 v62, v62
	v_mfma_f32_16x16x32_bf16 v[42:45], v[14:17], v[42:45], 0
	v_mfma_f32_16x16x32_bf16 v[50:53], v[26:29], v[138:141], v[50:53]
	v_mfma_f32_16x16x32_bf16 v[42:45], v[30:33], v[138:141], v[42:45]
	ds_read_b32 v139, v68
	v_lshl_add_u64 v[68:69], v[66:67], 0, s[4:5]
	v_add_co_u32_e32 v140, vcc, s13, v68
	s_waitcnt lgkmcnt(0)
	v_mul_f32_e32 v58, v139, v58
	v_addc_co_u32_e32 v141, vcc, 0, v69, vcc
	global_load_dword v138, v[140:141], off
	v_exp_f32_e32 v140, v58
	v_mul_f32_e32 v59, v139, v59
	v_exp_f32_e32 v59, v59
	v_mul_f32_e32 v60, v139, v60
	v_fma_f32 v58, -v140, v140, 1.0
	v_sqrt_f32_e32 v58, v58
	v_exp_f32_e32 v60, v60
	v_mul_f32_e32 v61, v139, v61
	v_exp_f32_e32 v61, v61
	v_mul_f32_e32 v58, v62, v58
	v_fmamk_f32 v62, v63, 0xbfb8aa3b, v137
	v_exp_f32_e32 v62, v62
	v_fma_f32 v63, -v59, v59, 1.0
	v_sqrt_f32_e32 v63, v63
	v_mul_f32_e32 v58, v119, v58
	v_add_f32_e32 v62, 1.0, v62
	v_rcp_f32_e32 v62, v62
	s_nop 0
	v_mul_f32_e32 v62, v62, v63
	v_fmamk_f32 v63, v64, 0xbfb8aa3b, v137
	v_exp_f32_e32 v63, v63
	v_fma_f32 v64, -v60, v60, 1.0
	v_sqrt_f32_e32 v64, v64
	v_add_f32_e32 v63, 1.0, v63
	v_rcp_f32_e32 v63, v63
	s_nop 0
	v_mul_f32_e32 v63, v63, v64
	v_fmamk_f32 v64, v65, 0xbfb8aa3b, v137
	v_exp_f32_e32 v64, v64
	v_fma_f32 v65, -v61, v61, 1.0
	v_sqrt_f32_e32 v65, v65
	v_add_f32_e32 v64, 1.0, v64
	v_rcp_f32_e32 v64, v64
	s_nop 0
	v_mul_f32_e32 v64, v64, v65
	v_mul_f32_e32 v65, v59, v140
	v_mul_f32_e32 v59, v59, v58
	v_fmac_f32_e32 v59, v120, v62
	v_mul_f32_e32 v141, v60, v65
	v_mul_f32_e32 v60, v60, v59
	v_fmac_f32_e32 v60, v121, v63
	v_mul_f32_e32 v142, v61, v141
	v_mul_f32_e32 v61, v61, v60
	v_fmac_f32_e32 v61, v122, v64
	ds_bpermute_b32 v62, v98, v142
	ds_bpermute_b32 v63, v98, v61
	ds_bpermute_b32 v64, v99, v142
	ds_bpermute_b32 v144, v99, v61
	ds_bpermute_b32 v145, v100, v142
	ds_bpermute_b32 v146, v100, v61
	ds_bpermute_b32 v147, v101, v142
	ds_bpermute_b32 v148, v101, v61
	s_waitcnt vmcnt(0) lgkmcnt(6)
	v_fmac_f32_e32 v63, v138, v62
	v_cndmask_b32_e64 v62, v138, v63, s[42:43]
	s_waitcnt lgkmcnt(4)
	v_fmac_f32_e32 v144, v63, v64
	v_cndmask_b32_e64 v62, v62, v144, s[44:45]
	s_waitcnt lgkmcnt(2)
	v_fmac_f32_e32 v146, v144, v145
	v_cndmask_b32_e64 v62, v62, v146, s[46:47]
	s_waitcnt lgkmcnt(0)
	v_fmac_f32_e32 v148, v146, v147
	v_fmac_f32_e32 v58, v140, v62
	v_fmac_f32_e32 v59, v65, v62
	v_fmac_f32_e32 v60, v141, v62
	v_fmac_f32_e32 v61, v142, v62
	v_fmamk_f32 v46, v46, 0xbfb8aa3b, v143
	v_exp_f32_e32 v46, v46
	v_fmamk_f32 v47, v47, 0xbfb8aa3b, v143
	v_exp_f32_e32 v47, v47
	v_fmamk_f32 v48, v48, 0xbfb8aa3b, v143
	v_add_f32_e32 v46, 1.0, v46
	v_rcp_f32_e64 v46, -v46
	v_exp_f32_e32 v48, v48
	v_fmamk_f32 v49, v49, 0xbfb8aa3b, v143
	v_exp_f32_e32 v49, v49
	v_fmamk_f32 v54, v54, 0xbfb8aa3b, v137
	v_mul_f32_e32 v46, v139, v46
	v_add_f32_e32 v47, 1.0, v47
	v_exp_f32_e32 v54, v54
	v_exp_f32_e32 v46, v46
	v_rcp_f32_e64 v47, -v47
	v_add_f32_e32 v48, 1.0, v48
	v_rcp_f32_e64 v48, -v48
	v_add_f32_e32 v49, 1.0, v49
	v_rcp_f32_e64 v49, -v49
	v_fmamk_f32 v55, v55, 0xbfb8aa3b, v137
	v_add_f32_e32 v54, 1.0, v54
	v_fma_f32 v62, -v46, v46, 1.0
	v_mul_f32_e32 v47, v139, v47
	v_rcp_f32_e32 v54, v54
	v_sqrt_f32_e32 v62, v62
	v_exp_f32_e32 v55, v55
	v_exp_f32_e32 v47, v47
	v_fmamk_f32 v56, v56, 0xbfb8aa3b, v137
	v_mul_f32_e32 v48, v139, v48
	v_exp_f32_e32 v56, v56
	v_exp_f32_e32 v48, v48
	v_fmamk_f32 v57, v57, 0xbfb8aa3b, v137
	v_mul_f32_e32 v49, v139, v49
	v_exp_f32_e32 v57, v57
	v_exp_f32_e32 v49, v49
	v_mul_f32_e32 v54, v54, v62
	v_add_f32_e32 v55, 1.0, v55
	v_fma_f32 v62, -v47, v47, 1.0
	v_rcp_f32_e32 v55, v55
	v_sqrt_f32_e32 v63, v62
	v_add_f32_e32 v56, 1.0, v56
	v_fma_f32 v62, -v48, v48, 1.0
	v_rcp_f32_e32 v56, v56
	v_sqrt_f32_e32 v64, v62
	v_add_f32_e32 v57, 1.0, v57
	v_fma_f32 v62, -v49, v49, 1.0
	v_rcp_f32_e32 v57, v57
	v_sqrt_f32_e32 v65, v62
	v_mul_f32_e32 v62, v123, v54
	v_mul_f32_e32 v54, v55, v63
	v_mul_f32_e32 v63, v47, v62
	v_fmac_f32_e32 v63, v124, v54
	v_mul_f32_e32 v55, v56, v64
	v_mul_f32_e32 v64, v48, v63
	v_mul_f32_e32 v56, v57, v65
	v_mul_f32_e32 v57, v47, v46
	v_fmac_f32_e32 v64, v125, v55
	v_mul_f32_e32 v138, v48, v57
	v_mul_f32_e32 v65, v49, v64
	v_mul_f32_e32 v140, v49, v138
	v_fmac_f32_e32 v65, v126, v56
	ds_bpermute_b32 v47, v98, v140
	ds_bpermute_b32 v48, v98, v65
	ds_bpermute_b32 v49, v99, v140
	ds_bpermute_b32 v54, v99, v65
	ds_bpermute_b32 v55, v100, v140
	ds_bpermute_b32 v56, v100, v65
	ds_bpermute_b32 v141, v101, v140
	ds_bpermute_b32 v144, v101, v65
	s_waitcnt lgkmcnt(6)
	v_fmac_f32_e32 v48, v148, v47
	v_cndmask_b32_e64 v47, v148, v48, s[42:43]
	s_waitcnt lgkmcnt(4)
	v_fmac_f32_e32 v54, v48, v49
	v_cndmask_b32_e64 v47, v47, v54, s[44:45]
	s_waitcnt lgkmcnt(2)
	v_fmac_f32_e32 v56, v54, v55
	v_cndmask_b32_e64 v47, v47, v56, s[46:47]
	s_waitcnt lgkmcnt(0)
	v_fmac_f32_e32 v144, v56, v141
	v_fmac_f32_e32 v62, v46, v47
	v_fmac_f32_e32 v63, v57, v47
	v_fmac_f32_e32 v64, v138, v47
	v_fmac_f32_e32 v65, v140, v47
	v_fmamk_f32 v38, v38, 0xbfb8aa3b, v143
	v_exp_f32_e32 v38, v38
	v_fmamk_f32 v39, v39, 0xbfb8aa3b, v143
	v_exp_f32_e32 v39, v39
	v_fmamk_f32 v40, v40, 0xbfb8aa3b, v143
	v_add_f32_e32 v38, 1.0, v38
	v_rcp_f32_e64 v38, -v38
	v_exp_f32_e32 v40, v40
	v_fmamk_f32 v41, v41, 0xbfb8aa3b, v143
	v_fmamk_f32 v46, v50, 0xbfb8aa3b, v137
	v_mul_f32_e32 v38, v139, v38
	v_add_f32_e32 v39, 1.0, v39
	v_exp_f32_e32 v41, v41
	v_exp_f32_e32 v46, v46
	v_exp_f32_e32 v38, v38
	v_rcp_f32_e64 v39, -v39
	v_add_f32_e32 v40, 1.0, v40
	v_rcp_f32_e64 v40, -v40
	v_add_f32_e32 v41, 1.0, v41
	v_fmamk_f32 v47, v51, 0xbfb8aa3b, v137
	v_add_f32_e32 v46, 1.0, v46
	v_fma_f32 v48, -v38, v38, 1.0
	v_mul_f32_e32 v39, v139, v39
	v_rcp_f32_e64 v41, -v41
	v_rcp_f32_e32 v46, v46
	v_sqrt_f32_e32 v48, v48
	v_exp_f32_e32 v47, v47
	v_exp_f32_e32 v39, v39
	v_fmamk_f32 v49, v52, 0xbfb8aa3b, v137
	v_mul_f32_e32 v40, v139, v40
	v_exp_f32_e32 v49, v49
	v_exp_f32_e32 v40, v40
	v_fmamk_f32 v51, v53, 0xbfb8aa3b, v137
	v_mul_f32_e32 v41, v139, v41
	v_mul_f32_e32 v46, v46, v48
	v_add_f32_e32 v47, 1.0, v47
	v_fma_f32 v48, -v39, v39, 1.0
	v_exp_f32_e32 v51, v51
	v_exp_f32_e32 v41, v41
	v_rcp_f32_e32 v47, v47
	v_sqrt_f32_e32 v48, v48
	v_add_f32_e32 v49, 1.0, v49
	v_fma_f32 v50, -v40, v40, 1.0
	v_rcp_f32_e32 v49, v49
	v_sqrt_f32_e32 v50, v50
	v_add_f32_e32 v51, 1.0, v51
	v_fma_f32 v52, -v41, v41, 1.0
	v_mul_f32_e32 v138, v129, v46
	v_rcp_f32_e32 v51, v51
	v_sqrt_f32_e32 v52, v52
	v_mul_f32_e32 v46, v47, v48
	v_mul_f32_e32 v140, v39, v138
	v_fmac_f32_e32 v140, v130, v46
	v_mul_f32_e32 v47, v49, v50
	v_mul_f32_e32 v141, v40, v140
	v_mul_f32_e32 v49, v39, v38
	v_fmac_f32_e32 v141, v131, v47
	v_mul_f32_e32 v48, v51, v52
	v_mul_f32_e32 v50, v40, v49
	v_mul_f32_e32 v142, v41, v141
	v_mul_f32_e32 v51, v41, v50
	v_fmac_f32_e32 v142, v132, v48
	ds_bpermute_b32 v39, v98, v51
	ds_bpermute_b32 v40, v98, v142
	ds_bpermute_b32 v41, v99, v51
	ds_bpermute_b32 v46, v99, v142
	ds_bpermute_b32 v47, v100, v51
	ds_bpermute_b32 v48, v100, v142
	ds_bpermute_b32 v52, v101, v51
	ds_bpermute_b32 v53, v101, v142
	s_waitcnt lgkmcnt(6)
	v_fmac_f32_e32 v40, v144, v39
	v_cndmask_b32_e64 v39, v144, v40, s[42:43]
	s_waitcnt lgkmcnt(4)
	v_fmac_f32_e32 v46, v40, v41
	v_cndmask_b32_e64 v39, v39, v46, s[44:45]
	s_waitcnt lgkmcnt(2)
	v_fmac_f32_e32 v48, v46, v47
	v_cndmask_b32_e64 v39, v39, v48, s[46:47]
	s_waitcnt lgkmcnt(0)
	v_fmac_f32_e32 v53, v48, v52
	v_fmac_f32_e32 v138, v38, v39
	v_fmac_f32_e32 v140, v49, v39
	v_fmac_f32_e32 v141, v50, v39
	v_fmac_f32_e32 v142, v51, v39
	v_fmamk_f32 v34, v34, 0xbfb8aa3b, v143
	v_exp_f32_e32 v34, v34
	v_fmamk_f32 v35, v35, 0xbfb8aa3b, v143
	v_exp_f32_e32 v35, v35
	v_fmamk_f32 v36, v36, 0xbfb8aa3b, v143
	v_add_f32_e32 v34, 1.0, v34
	v_rcp_f32_e64 v34, -v34
	v_exp_f32_e32 v36, v36
	v_fmac_f32_e32 v143, 0xbfb8aa3b, v37
	v_fmamk_f32 v38, v42, 0xbfb8aa3b, v137
	v_mul_f32_e32 v34, v139, v34
	v_add_f32_e32 v35, 1.0, v35
	v_exp_f32_e32 v37, v143
	v_exp_f32_e32 v38, v38
	v_exp_f32_e32 v34, v34
	v_rcp_f32_e64 v35, -v35
	v_add_f32_e32 v36, 1.0, v36
	v_rcp_f32_e64 v36, -v36
	v_add_f32_e32 v37, 1.0, v37
	v_fmamk_f32 v39, v43, 0xbfb8aa3b, v137
	v_add_f32_e32 v38, 1.0, v38
	v_fma_f32 v40, -v34, v34, 1.0
	v_mul_f32_e32 v35, v139, v35
	v_rcp_f32_e64 v37, -v37
	v_rcp_f32_e32 v38, v38
	v_sqrt_f32_e32 v40, v40
	v_exp_f32_e32 v39, v39
	v_exp_f32_e32 v35, v35
	v_fmamk_f32 v41, v44, 0xbfb8aa3b, v137
	v_mul_f32_e32 v36, v139, v36
	v_exp_f32_e32 v41, v41
	v_exp_f32_e32 v36, v36
	v_fmac_f32_e32 v137, 0xbfb8aa3b, v45
	v_mul_f32_e32 v37, v139, v37
	v_mul_f32_e32 v38, v38, v40
	v_add_f32_e32 v39, 1.0, v39
	v_fma_f32 v40, -v35, v35, 1.0
	v_exp_f32_e32 v43, v137
	v_exp_f32_e32 v37, v37
	v_rcp_f32_e32 v39, v39
	v_sqrt_f32_e32 v40, v40
	v_add_f32_e32 v41, 1.0, v41
	v_fma_f32 v42, -v36, v36, 1.0
	v_rcp_f32_e32 v41, v41
	v_sqrt_f32_e32 v42, v42
	v_add_f32_e32 v43, 1.0, v43
	v_fma_f32 v44, -v37, v37, 1.0
	v_mul_f32_e32 v139, v133, v38
	v_rcp_f32_e32 v43, v43
	v_sqrt_f32_e32 v44, v44
	v_mul_f32_e32 v38, v39, v40
	v_mul_f32_e32 v143, v35, v139
	v_fmac_f32_e32 v143, v134, v38
	v_mul_f32_e32 v39, v41, v42
	v_mul_f32_e32 v156, v36, v143
	v_mul_f32_e32 v41, v35, v34
	v_fmac_f32_e32 v156, v135, v39
	v_mul_f32_e32 v40, v43, v44
	v_mul_f32_e32 v42, v36, v41
	v_mul_f32_e32 v157, v37, v156
	v_mul_f32_e32 v43, v37, v42
	v_fmac_f32_e32 v157, v127, v40
	ds_bpermute_b32 v35, v98, v43
	ds_bpermute_b32 v36, v98, v157
	ds_bpermute_b32 v37, v99, v43
	ds_bpermute_b32 v38, v99, v157
	ds_bpermute_b32 v39, v100, v43
	ds_bpermute_b32 v40, v100, v157
	s_waitcnt lgkmcnt(4)
	v_fmac_f32_e32 v36, v53, v35
	v_cndmask_b32_e64 v35, v53, v36, s[42:43]
	s_waitcnt lgkmcnt(2)
	v_fmac_f32_e32 v38, v36, v37
	v_cndmask_b32_e64 v35, v35, v38, s[44:45]
	s_waitcnt lgkmcnt(0)
	v_fmac_f32_e32 v40, v38, v39
	v_cndmask_b32_e64 v35, v35, v40, s[46:47]
	v_fmac_f32_e32 v139, v34, v35
	v_fmac_f32_e32 v143, v41, v35
	v_fmac_f32_e32 v156, v42, v35
	v_fmac_f32_e32 v157, v43, v35
	s_mov_b32 s13, 0x7b720000
	v_add_co_u32_e32 v68, vcc, s13, v68
	v_add_u32_e32 v34, 0x17a00, v136
	v_add_u32_e32 v38, 0x17a40, v136
	v_add_u32_e32 v50, 0x19e00, v136
	v_add_u32_e32 v51, 0x19e40, v136
	v_add_u32_e32 v136, 0x1c800, v128
	v_addc_co_u32_e32 v69, vcc, 0, v69, vcc
	ds_read_b128 v[34:37], v34
	ds_read_b128 v[46:49], v38
	ds_read_b128 v[54:57], v50
	ds_read_b128 v[144:147], v51
	v_add_u32_e32 v152, 0x1ca00, v128
	v_add_u32_e32 v153, 0x1cc00, v128
	ds_read_b32 v137, v136
	ds_read_b32 v128, v152
	ds_read_b32 v136, v153
	global_load_dword v68, v[68:69], off
	s_waitcnt lgkmcnt(6)
	v_mfma_f32_16x16x32_bf16 v[50:53], v[14:17], v[34:37], 0
	s_waitcnt lgkmcnt(5)
	v_mfma_f32_16x16x32_bf16 v[148:151], v[30:33], v[46:49], v[50:53]
	s_waitcnt lgkmcnt(4)
	v_mfma_f32_16x16x32_bf16 v[50:53], v[14:17], v[54:57], 0
	s_waitcnt lgkmcnt(3)
	v_mfma_f32_16x16x32_bf16 v[152:155], v[30:33], v[144:147], v[50:53]
	s_waitcnt lgkmcnt(2)
	s_nop 2
	v_fmamk_f32 v69, v148, 0xbfb8aa3b, v137
	v_fmamk_f32 v150, v150, 0xbfb8aa3b, v137
	v_exp_f32_e32 v150, v150
	v_exp_f32_e32 v50, v69
	v_mfma_f32_16x16x32_bf16 v[38:41], v[2:5], v[34:37], 0
	s_waitcnt lgkmcnt(1)
	v_fmamk_f32 v51, v152, 0xbfb8aa3b, v128
	v_exp_f32_e32 v51, v51
	v_add_f32_e32 v50, 1.0, v50
	v_rcp_f32_e64 v50, -v50
	v_mfma_f32_16x16x32_bf16 v[42:45], v[6:9], v[34:37], 0
	v_add_f32_e32 v51, 1.0, v51
	v_rcp_f32_e32 v69, v51
	s_waitcnt lgkmcnt(0)
	v_mul_f32_e32 v50, v136, v50
	v_mfma_f32_16x16x32_bf16 v[34:37], v[10:13], v[34:37], 0
	v_exp_f32_e32 v148, v50
	v_fmamk_f32 v154, v154, 0xbfb8aa3b, v128
	v_exp_f32_e32 v154, v154
	v_mfma_f32_16x16x32_bf16 v[50:53], v[26:29], v[46:49], v[34:37]
	v_mfma_f32_16x16x32_bf16 v[38:41], v[18:21], v[46:49], v[38:41]
	s_nop 2
	v_fmamk_f32 v34, v149, 0xbfb8aa3b, v137
	v_mfma_f32_16x16x32_bf16 v[42:45], v[22:25], v[46:49], v[42:45]
	v_exp_f32_e32 v46, v34
	v_fma_f32 v47, -v148, v148, 1.0
	v_sqrt_f32_e32 v149, v47
	v_fmamk_f32 v47, v153, 0xbfb8aa3b, v128
	v_add_f32_e32 v46, 1.0, v46
	v_rcp_f32_e64 v46, -v46
	v_mfma_f32_16x16x32_bf16 v[34:37], v[2:5], v[54:57], 0
	v_exp_f32_e32 v152, v47
	v_mul_f32_e32 v69, v69, v149
	v_mul_f32_e32 v153, v136, v46
	v_mfma_f32_16x16x32_bf16 v[46:49], v[6:9], v[54:57], 0
	v_exp_f32_e32 v153, v153
	v_add_f32_e32 v152, 1.0, v152
	v_rcp_f32_e32 v152, v152
	v_mfma_f32_16x16x32_bf16 v[54:57], v[10:13], v[54:57], 0
	v_fma_f32 v158, -v153, v153, 1.0
	v_sqrt_f32_e32 v158, v158
	v_mfma_f32_16x16x32_bf16 v[34:37], v[18:21], v[144:147], v[34:37]
	v_mul_f32_e32 v149, v152, v158
	v_mfma_f32_16x16x32_bf16 v[46:49], v[22:25], v[144:147], v[46:49]
	v_mfma_f32_16x16x32_bf16 v[54:57], v[26:29], v[144:147], v[54:57]
	v_fmamk_f32 v146, v151, 0xbfb8aa3b, v137
	v_exp_f32_e32 v146, v146
	v_add_f32_e32 v144, 1.0, v150
	v_rcp_f32_e64 v144, -v144
	v_fmamk_f32 v150, v155, 0xbfb8aa3b, v128
	v_add_f32_e32 v146, 1.0, v146
	v_rcp_f32_e64 v146, -v146
	v_mul_f32_e32 v144, v136, v144
	v_exp_f32_e32 v144, v144
	v_exp_f32_e32 v150, v150
	v_mul_f32_e32 v146, v136, v146
	v_exp_f32_e32 v146, v146
	v_add_f32_e32 v145, 1.0, v154
	v_fma_f32 v147, -v144, v144, 1.0
	v_add_f32_e32 v150, 1.0, v150
	v_fma_f32 v151, -v146, v146, 1.0
	v_rcp_f32_e32 v145, v145
	v_sqrt_f32_e32 v147, v147
	v_rcp_f32_e32 v150, v150
	v_sqrt_f32_e32 v151, v151
	v_mul_f32_e32 v145, v145, v147
	v_mul_f32_e32 v147, v150, v151
	v_mul_f32_e32 v147, v127, v147
	v_mul_f32_e32 v127, v144, v146
	v_mul_f32_e32 v144, v144, v147
	v_fmac_f32_e32 v144, v135, v145
	v_mul_f32_e32 v135, v153, v144
	v_fmac_f32_e32 v135, v134, v149
	v_mul_f32_e32 v150, v153, v127
	v_mul_f32_e32 v134, v148, v135
	v_mul_f32_e32 v151, v148, v150
	v_fmac_f32_e32 v134, v133, v69
	ds_bpermute_b32 v133, v101, v151
	ds_bpermute_b32 v148, v101, v134
	ds_bpermute_b32 v149, v100, v151
	ds_bpermute_b32 v152, v100, v134
	ds_bpermute_b32 v153, v99, v151
	ds_bpermute_b32 v154, v99, v134
	ds_bpermute_b32 v69, v98, v151
	ds_bpermute_b32 v145, v98, v134
	s_waitcnt vmcnt(0) lgkmcnt(6)
	v_fmac_f32_e32 v148, v68, v133
	v_cndmask_b32_e64 v68, v68, v148, s[44:45]
	s_waitcnt lgkmcnt(4)
	v_fmac_f32_e32 v152, v148, v149
	v_cndmask_b32_e64 v68, v68, v152, s[42:43]
	s_waitcnt lgkmcnt(2)
	v_fmac_f32_e32 v154, v152, v153
	v_cndmask_b32_e64 v133, v68, v154, s[40:41]
	v_fmac_f32_e32 v134, v151, v133
	v_fmac_f32_e32 v135, v150, v133
	v_fmac_f32_e32 v144, v127, v133
	v_fmac_f32_e32 v147, v146, v133
	s_waitcnt lgkmcnt(0)
	v_fmac_f32_e32 v145, v154, v69
	v_add_f32_e32 v68, v139, v134
	v_add_f32_e32 v69, v143, v135
	v_add_f32_e32 v127, v156, v144
	v_add_f32_e32 v133, v157, v147
	v_fmamk_f32 v50, v50, 0xbfb8aa3b, v137
	v_exp_f32_e32 v50, v50
	v_fmamk_f32 v51, v51, 0xbfb8aa3b, v137
	v_exp_f32_e32 v51, v51
	v_fmamk_f32 v54, v54, 0xbfb8aa3b, v128
	v_add_f32_e32 v50, 1.0, v50
	v_rcp_f32_e64 v50, -v50
	v_add_f32_e32 v51, 1.0, v51
	v_fmamk_f32 v52, v52, 0xbfb8aa3b, v137
	v_exp_f32_e32 v54, v54
	v_mul_f32_e32 v50, v136, v50
	v_exp_f32_e32 v50, v50
	v_rcp_f32_e64 v51, -v51
	v_exp_f32_e32 v52, v52
	v_add_f32_e32 v54, 1.0, v54
	v_fma_f32 v134, -v50, v50, 1.0
	v_fmamk_f32 v55, v55, 0xbfb8aa3b, v128
	v_mul_f32_e32 v51, v136, v51
	v_add_f32_e32 v52, 1.0, v52
	v_fmamk_f32 v53, v53, 0xbfb8aa3b, v137
	v_rcp_f32_e32 v54, v54
	v_sqrt_f32_e32 v134, v134
	v_exp_f32_e32 v55, v55
	v_exp_f32_e32 v51, v51
	v_rcp_f32_e64 v52, -v52
	v_exp_f32_e32 v53, v53
	v_mul_f32_e32 v54, v54, v134
	v_add_f32_e32 v55, 1.0, v55
	v_fma_f32 v134, -v51, v51, 1.0
	v_fmamk_f32 v56, v56, 0xbfb8aa3b, v128
	v_mul_f32_e32 v52, v136, v52
	v_add_f32_e32 v53, 1.0, v53
	v_rcp_f32_e32 v55, v55
	v_sqrt_f32_e32 v134, v134
	v_exp_f32_e32 v56, v56
	v_exp_f32_e32 v52, v52
	v_rcp_f32_e64 v53, -v53
	v_mul_f32_e32 v55, v55, v134
	v_add_f32_e32 v56, 1.0, v56
	v_fma_f32 v134, -v52, v52, 1.0
	v_fmamk_f32 v57, v57, 0xbfb8aa3b, v128
	v_mul_f32_e32 v53, v136, v53
	v_rcp_f32_e32 v56, v56
	v_sqrt_f32_e32 v134, v134
	v_exp_f32_e32 v57, v57
	v_exp_f32_e32 v53, v53
	v_mul_f32_e32 v56, v56, v134
	v_add_f32_e32 v57, 1.0, v57
	v_fma_f32 v134, -v53, v53, 1.0
	v_rcp_f32_e32 v57, v57
	v_sqrt_f32_e32 v134, v134
	s_nop 0
	v_mul_f32_e32 v57, v57, v134
	v_mul_f32_e32 v57, v132, v57
	v_mul_f32_e32 v132, v52, v53
	v_mul_f32_e32 v52, v52, v57
	v_fmac_f32_e32 v52, v131, v56
	v_mul_f32_e32 v134, v51, v132
	v_mul_f32_e32 v51, v51, v52
	v_fmac_f32_e32 v51, v130, v55
	v_mul_f32_e32 v135, v50, v134
	v_mul_f32_e32 v50, v50, v51
	v_fmac_f32_e32 v50, v129, v54
	ds_bpermute_b32 v139, v101, v135
	ds_bpermute_b32 v143, v101, v50
	ds_bpermute_b32 v130, v100, v135
	ds_bpermute_b32 v131, v100, v50
	ds_bpermute_b32 v56, v99, v135
	ds_bpermute_b32 v129, v99, v50
	ds_bpermute_b32 v54, v98, v135
	ds_bpermute_b32 v55, v98, v50
	s_waitcnt lgkmcnt(6)
	v_fmac_f32_e32 v143, v145, v139
	v_cndmask_b32_e64 v139, v145, v143, s[44:45]
	s_waitcnt lgkmcnt(4)
	v_fmac_f32_e32 v131, v143, v130
	v_cndmask_b32_e64 v130, v139, v131, s[42:43]
	s_waitcnt lgkmcnt(2)
	v_fmac_f32_e32 v129, v131, v56
	v_cndmask_b32_e64 v56, v130, v129, s[40:41]
	v_fmac_f32_e32 v50, v135, v56
	v_fmac_f32_e32 v51, v134, v56
	v_fmac_f32_e32 v52, v132, v56
	v_fmac_f32_e32 v57, v53, v56
	s_waitcnt lgkmcnt(0)
	v_fmac_f32_e32 v55, v129, v54
	v_add_f32_e32 v50, v138, v50
	v_add_f32_e32 v51, v140, v51
	v_add_f32_e32 v52, v141, v52
	v_add_f32_e32 v53, v142, v57
	v_fmamk_f32 v42, v42, 0xbfb8aa3b, v137
	v_exp_f32_e32 v42, v42
	v_fmamk_f32 v43, v43, 0xbfb8aa3b, v137
	v_exp_f32_e32 v43, v43
	v_fmamk_f32 v46, v46, 0xbfb8aa3b, v128
	v_add_f32_e32 v42, 1.0, v42
	v_rcp_f32_e64 v42, -v42
	v_add_f32_e32 v43, 1.0, v43
	v_fmamk_f32 v44, v44, 0xbfb8aa3b, v137
	v_exp_f32_e32 v46, v46
	v_mul_f32_e32 v42, v136, v42
	v_exp_f32_e32 v42, v42
	v_rcp_f32_e64 v43, -v43
	v_exp_f32_e32 v44, v44
	v_add_f32_e32 v46, 1.0, v46
	v_fma_f32 v54, -v42, v42, 1.0
	v_fmamk_f32 v47, v47, 0xbfb8aa3b, v128
	v_mul_f32_e32 v43, v136, v43
	v_add_f32_e32 v44, 1.0, v44
	v_fmamk_f32 v45, v45, 0xbfb8aa3b, v137
	v_rcp_f32_e32 v46, v46
	v_sqrt_f32_e32 v54, v54
	v_exp_f32_e32 v47, v47
	v_exp_f32_e32 v43, v43
	v_rcp_f32_e64 v44, -v44
	v_exp_f32_e32 v45, v45
	v_mul_f32_e32 v46, v46, v54
	v_add_f32_e32 v47, 1.0, v47
	v_fma_f32 v54, -v43, v43, 1.0
	v_fmamk_f32 v48, v48, 0xbfb8aa3b, v128
	v_mul_f32_e32 v44, v136, v44
	v_add_f32_e32 v45, 1.0, v45
	v_rcp_f32_e32 v47, v47
	v_sqrt_f32_e32 v54, v54
	v_exp_f32_e32 v48, v48
	v_exp_f32_e32 v44, v44
	v_rcp_f32_e64 v45, -v45
	v_mul_f32_e32 v47, v47, v54
	v_add_f32_e32 v48, 1.0, v48
	v_fma_f32 v54, -v44, v44, 1.0
	v_fmamk_f32 v49, v49, 0xbfb8aa3b, v128
	v_mul_f32_e32 v45, v136, v45
	v_rcp_f32_e32 v48, v48
	v_sqrt_f32_e32 v54, v54
	v_exp_f32_e32 v49, v49
	v_exp_f32_e32 v45, v45
	v_mul_f32_e32 v48, v48, v54
	v_add_f32_e32 v49, 1.0, v49
	v_fma_f32 v54, -v45, v45, 1.0
	v_rcp_f32_e32 v49, v49
	v_sqrt_f32_e32 v54, v54
	s_nop 0
	v_mul_f32_e32 v49, v49, v54
	v_mul_f32_e32 v49, v126, v49
	v_mul_f32_e32 v54, v44, v45
	v_mul_f32_e32 v44, v44, v49
	v_fmac_f32_e32 v44, v125, v48
	v_mul_f32_e32 v56, v43, v54
	v_mul_f32_e32 v43, v43, v44
	v_fmac_f32_e32 v43, v124, v47
	v_mul_f32_e32 v57, v42, v56
	v_mul_f32_e32 v42, v42, v43
	v_fmac_f32_e32 v42, v123, v46
	ds_bpermute_b32 v126, v101, v57
	ds_bpermute_b32 v129, v101, v42
	ds_bpermute_b32 v124, v100, v57
	ds_bpermute_b32 v125, v100, v42
	ds_bpermute_b32 v48, v99, v57
	ds_bpermute_b32 v123, v99, v42
	ds_bpermute_b32 v46, v98, v57
	ds_bpermute_b32 v47, v98, v42
	s_waitcnt lgkmcnt(6)
	v_fmac_f32_e32 v129, v55, v126
	v_cndmask_b32_e64 v55, v55, v129, s[44:45]
	s_waitcnt lgkmcnt(4)
	v_fmac_f32_e32 v125, v129, v124
	v_cndmask_b32_e64 v55, v55, v125, s[42:43]
	s_waitcnt lgkmcnt(2)
	v_fmac_f32_e32 v123, v125, v48
	v_cndmask_b32_e64 v48, v55, v123, s[40:41]
	v_fmac_f32_e32 v42, v57, v48
	v_fmac_f32_e32 v43, v56, v48
	v_fmac_f32_e32 v44, v54, v48
	v_fmac_f32_e32 v49, v45, v48
	s_waitcnt lgkmcnt(0)
	v_fmac_f32_e32 v47, v123, v46
	v_add_f32_e32 v42, v62, v42
	v_add_f32_e32 v43, v63, v43
	v_add_f32_e32 v44, v64, v44
	v_add_f32_e32 v45, v65, v49
	v_fmamk_f32 v38, v38, 0xbfb8aa3b, v137
	v_exp_f32_e32 v38, v38
	v_fmamk_f32 v39, v39, 0xbfb8aa3b, v137
	v_exp_f32_e32 v39, v39
	v_fmamk_f32 v40, v40, 0xbfb8aa3b, v137
	v_add_f32_e32 v38, 1.0, v38
	v_rcp_f32_e64 v38, -v38
	v_add_f32_e32 v39, 1.0, v39
	v_fmamk_f32 v34, v34, 0xbfb8aa3b, v128
	v_rcp_f32_e64 v39, -v39
	v_mul_f32_e32 v38, v136, v38
	v_exp_f32_e32 v38, v38
	v_exp_f32_e32 v40, v40
	v_exp_f32_e32 v34, v34
	v_mul_f32_e32 v39, v136, v39
	v_fmac_f32_e32 v137, 0xbfb8aa3b, v41
	v_add_f32_e32 v40, 1.0, v40
	v_add_f32_e32 v34, 1.0, v34
	v_fma_f32 v54, -v38, v38, 1.0
	v_fmamk_f32 v35, v35, 0xbfb8aa3b, v128
	v_exp_f32_e32 v39, v39
	v_rcp_f32_e64 v40, -v40
	v_exp_f32_e32 v41, v137
	v_rcp_f32_e32 v34, v34
	v_sqrt_f32_e32 v54, v54
	v_exp_f32_e32 v35, v35
	v_mul_f32_e32 v40, v136, v40
	v_add_f32_e32 v41, 1.0, v41
	v_mul_f32_e32 v34, v34, v54
	v_add_f32_e32 v35, 1.0, v35
	v_fma_f32 v54, -v39, v39, 1.0
	v_fmamk_f32 v36, v36, 0xbfb8aa3b, v128
	v_exp_f32_e32 v40, v40
	v_rcp_f32_e64 v41, -v41
	v_rcp_f32_e32 v35, v35
	v_sqrt_f32_e32 v54, v54
	v_exp_f32_e32 v36, v36
	v_mul_f32_e32 v41, v136, v41
	v_fmac_f32_e32 v128, 0xbfb8aa3b, v37
	v_mul_f32_e32 v35, v35, v54
	v_add_f32_e32 v36, 1.0, v36
	v_fma_f32 v54, -v40, v40, 1.0
	v_exp_f32_e32 v41, v41
	v_rcp_f32_e32 v36, v36
	v_sqrt_f32_e32 v54, v54
	v_exp_f32_e32 v37, v128
	v_mul_f32_e32 v46, v40, v41
	v_mul_f32_e32 v48, v39, v46
	v_mul_f32_e32 v36, v36, v54
	v_add_f32_e32 v37, 1.0, v37
	v_fma_f32 v54, -v41, v41, 1.0
	v_rcp_f32_e32 v37, v37
	v_sqrt_f32_e32 v54, v54
	v_mul_f32_e32 v49, v38, v48
	ds_bpermute_b32 v55, v101, v49
	v_mul_f32_e32 v37, v37, v54
	v_mul_f32_e32 v37, v122, v37
	v_mul_f32_e32 v40, v40, v37
	v_fmac_f32_e32 v40, v121, v36
	v_mul_f32_e32 v36, v39, v40
	v_fmac_f32_e32 v36, v120, v35
	v_mul_f32_e32 v35, v38, v36
	v_fmac_f32_e32 v35, v119, v34
	ds_bpermute_b32 v56, v101, v35
	ds_bpermute_b32 v39, v100, v49
	ds_bpermute_b32 v54, v100, v35
	ds_bpermute_b32 v34, v99, v49
	ds_bpermute_b32 v38, v99, v35
	s_waitcnt lgkmcnt(4)
	v_fmac_f32_e32 v56, v47, v55
	v_cndmask_b32_e64 v47, v47, v56, s[44:45]
	s_waitcnt lgkmcnt(2)
	v_fmac_f32_e32 v54, v56, v39
	v_cndmask_b32_e64 v39, v47, v54, s[42:43]
	s_waitcnt lgkmcnt(0)
	v_fmac_f32_e32 v38, v54, v34
	v_cndmask_b32_e64 v34, v39, v38, s[40:41]
	v_fmac_f32_e32 v35, v49, v34
	v_fmac_f32_e32 v36, v48, v34
	v_fmac_f32_e32 v40, v46, v34
	v_fmac_f32_e32 v37, v41, v34
	v_add_f32_e32 v35, v58, v35
	v_add_f32_e32 v36, v59, v36
	v_add_f32_e32 v38, v60, v40
	v_add_f32_e32 v34, v61, v37
	v_cvt_pk_bf16_f32 v34, v34, s0
	ds_write_b16 v118, v34 offset:720
	v_cvt_pk_bf16_f32 v34, v42, s0
	ds_write_b16 v118, v34 offset:2592
	v_cvt_pk_bf16_f32 v34, v43, s0
	ds_write_b16 v118, v34 offset:2736
	v_cvt_pk_bf16_f32 v34, v44, s0
	ds_write_b16 v118, v34 offset:2880
	v_cvt_pk_bf16_f32 v34, v45, s0
	ds_write_b16 v118, v34 offset:3024
	v_cvt_pk_bf16_f32 v34, v50, s0
	ds_write_b16 v118, v34 offset:4896
	v_cvt_pk_bf16_f32 v34, v51, s0
	ds_write_b16 v118, v34 offset:5040
	v_cvt_pk_bf16_f32 v34, v52, s0
	ds_write_b16 v118, v34 offset:5184
	v_cvt_pk_bf16_f32 v34, v53, s0
	ds_write_b16 v118, v34 offset:5328
	v_cvt_pk_bf16_f32 v34, v68, s0
	v_cvt_pk_bf16_f32 v35, v35, s0
	ds_write_b16 v118, v34 offset:7200
	v_cvt_pk_bf16_f32 v34, v69, s0
	s_add_u32 s4, s4, 64
	ds_write_b16 v118, v35 offset:288
	v_cvt_pk_bf16_f32 v35, v36, s0
	ds_write_b16 v118, v34 offset:7344
	v_cvt_pk_bf16_f32 v34, v127, s0
	s_addc_u32 s5, s5, 0
	ds_write_b16 v118, v35 offset:432
	v_cvt_pk_bf16_f32 v35, v38, s0
	ds_write_b16 v118, v34 offset:7488
	v_cvt_pk_bf16_f32 v34, v133, s0
	v_add_u32_e32 v117, 64, v117
	v_add_u32_e32 v116, 0x900, v116
	s_cmpk_lg_i32 s4, 0x100
	v_add_u32_e32 v0, 32, v0
	ds_write_b16 v118, v35 offset:576
	ds_write_b16 v118, v34 offset:7632
	s_cbranch_scc1 .LBB0_621
	s_add_i32 s4, s9, s8
	v_or_b32_e32 v0, s4, v71
	s_movk_i32 s13, 0x2c00
	s_waitcnt lgkmcnt(0)
	v_or_b32_e32 v48, s4, v71
	v_mad_i64_i32 v[16:17], s[8:9], v48, s13, v[74:75]
	global_load_dwordx4 v[16:19], v[16:17], off offset:3072
	v_or_b32_e32 v48, s4, v79
	v_mad_i64_i32 v[20:21], s[8:9], v48, s13, v[74:75]
	global_load_dwordx4 v[20:23], v[20:21], off offset:3072
	v_or_b32_e32 v48, s4, v81
	v_mad_i64_i32 v[24:25], s[8:9], v48, s13, v[74:75]
	global_load_dwordx4 v[24:27], v[24:25], off offset:3072
	v_or_b32_e32 v48, s4, v83
	v_mad_i64_i32 v[28:29], s[8:9], v48, s13, v[74:75]
	global_load_dwordx4 v[28:31], v[28:29], off offset:3072
	v_or_b32_e32 v48, s4, v85
	v_mad_i64_i32 v[32:33], s[8:9], v48, s13, v[74:75]
	global_load_dwordx4 v[32:35], v[32:33], off offset:3072
	v_or_b32_e32 v48, s4, v87
	v_mad_i64_i32 v[36:37], s[8:9], v48, s13, v[74:75]
	global_load_dwordx4 v[36:39], v[36:37], off offset:3072
	v_or_b32_e32 v48, s4, v89
	v_mad_i64_i32 v[40:41], s[8:9], v48, s13, v[74:75]
	global_load_dwordx4 v[40:43], v[40:41], off offset:3072
	v_or_b32_e32 v48, s4, v91
	v_mad_i64_i32 v[44:45], s[8:9], v48, s13, v[74:75]
	global_load_dwordx4 v[44:47], v[44:45], off offset:3072
	v_mad_i64_i32 v[6:7], s[8:9], v0, s13, v[74:75]
	ds_read_b128 v[2:5], v108 offset:288
	s_add_i32 s11, s11, s30
	s_cmp_lt_i32 s11, s10
	s_waitcnt lgkmcnt(0)
	v_lshlrev_b32_e32 v10, 16, v2
	v_and_b32_e32 v11, 0xffff0000, v2
	s_waitcnt vmcnt(7)
	v_mov_b32_e32 v6, v16
	v_mov_b32_e32 v7, v17
	v_mov_b32_e32 v8, v18
	v_mov_b32_e32 v9, v19
	v_lshlrev_b32_e32 v12, 16, v6
	v_mul_f32_e32 v2, 0x3d372713, v12
	v_and_b32_e32 v13, 0xffff0000, v6
	v_mul_f32_e32 v2, v2, v12
	v_mov_b32_e32 v6, v12
	v_fmac_f32_e32 v6, v2, v6
	v_mul_f32_e32 v2, 0x3f4c422a, v6
	v_add_f32_e32 v2, v2, v2
	v_mul_f32_e32 v2, 0xbfb8aa3b, v2
	v_exp_f32_e32 v2, v2
	v_mov_b32_e32 v6, v13
	v_add_f32_e32 v2, 1.0, v2
	v_rcp_f32_e32 v14, v2
	v_mul_f32_e32 v2, 0x3d372713, v13
	v_mul_f32_e32 v2, v2, v13
	v_fmac_f32_e32 v6, v2, v6
	v_mul_f32_e32 v2, 0x3f4c422a, v6
	v_add_f32_e32 v2, v2, v2
	v_mul_f32_e32 v2, 0xbfb8aa3b, v2
	v_exp_f32_e32 v2, v2
	v_lshlrev_b32_e32 v6, 16, v7
	v_and_b32_e32 v7, 0xffff0000, v7
	v_add_f32_e32 v2, 1.0, v2
	v_rcp_f32_e32 v15, v2
	s_nop 0
	v_pk_mul_f32 v[12:13], v[14:15], v[12:13]
	s_nop 0
	v_pk_mul_f32 v[10:11], v[12:13], v[10:11]
	v_mov_b32_e32 v12, v6
	v_cvt_pk_bf16_f32 v2, v10, v11
	v_lshlrev_b32_e32 v10, 16, v3
	v_and_b32_e32 v11, 0xffff0000, v3
	v_mul_f32_e32 v3, 0x3d372713, v6
	v_mul_f32_e32 v3, v3, v6
	v_fmac_f32_e32 v12, v3, v12
	v_mul_f32_e32 v3, 0x3f4c422a, v12
	v_add_f32_e32 v3, v3, v3
	v_mul_f32_e32 v3, 0xbfb8aa3b, v3
	v_exp_f32_e32 v3, v3
	v_mov_b32_e32 v13, v7
	v_add_f32_e32 v3, 1.0, v3
	v_rcp_f32_e32 v12, v3
	v_mul_f32_e32 v3, 0x3d372713, v7
	v_mul_f32_e32 v3, v3, v7
	v_fmac_f32_e32 v13, v3, v13
	v_mul_f32_e32 v3, 0x3f4c422a, v13
	v_add_f32_e32 v3, v3, v3
	v_mul_f32_e32 v3, 0xbfb8aa3b, v3
	v_exp_f32_e32 v3, v3
	s_nop 0
	v_add_f32_e32 v3, 1.0, v3
	v_rcp_f32_e32 v13, v3
	s_nop 0
	v_pk_mul_f32 v[6:7], v[12:13], v[6:7]
	s_nop 0
	v_pk_mul_f32 v[6:7], v[6:7], v[10:11]
	v_lshlrev_b32_e32 v10, 16, v8
	v_cvt_pk_bf16_f32 v3, v6, v7
	v_lshlrev_b32_e32 v6, 16, v4
	v_and_b32_e32 v7, 0xffff0000, v4
	v_mul_f32_e32 v4, 0x3d372713, v10
	v_and_b32_e32 v11, 0xffff0000, v8
	v_mul_f32_e32 v4, v4, v10
	v_mov_b32_e32 v8, v10
	v_fmac_f32_e32 v8, v4, v8
	v_mul_f32_e32 v4, 0x3f4c422a, v8
	v_add_f32_e32 v4, v4, v4
	v_mul_f32_e32 v4, 0xbfb8aa3b, v4
	v_exp_f32_e32 v4, v4
	v_mov_b32_e32 v8, v11
	v_add_f32_e32 v4, 1.0, v4
	v_rcp_f32_e32 v12, v4
	v_mul_f32_e32 v4, 0x3d372713, v11
	v_mul_f32_e32 v4, v4, v11
	v_fmac_f32_e32 v8, v4, v8
	v_mul_f32_e32 v4, 0x3f4c422a, v8
	v_add_f32_e32 v4, v4, v4
	v_mul_f32_e32 v4, 0xbfb8aa3b, v4
	v_exp_f32_e32 v4, v4
	v_lshlrev_b32_e32 v8, 16, v9
	v_and_b32_e32 v9, 0xffff0000, v9
	v_add_f32_e32 v4, 1.0, v4
	v_rcp_f32_e32 v13, v4
	s_nop 0
	v_pk_mul_f32 v[10:11], v[12:13], v[10:11]
	s_nop 0
	v_pk_mul_f32 v[6:7], v[10:11], v[6:7]
	v_mov_b32_e32 v10, v8
	v_cvt_pk_bf16_f32 v4, v6, v7
	v_lshlrev_b32_e32 v6, 16, v5
	v_and_b32_e32 v7, 0xffff0000, v5
	v_mul_f32_e32 v5, 0x3d372713, v8
	v_mul_f32_e32 v5, v5, v8
	v_fmac_f32_e32 v10, v5, v10
	v_mul_f32_e32 v5, 0x3f4c422a, v10
	v_add_f32_e32 v5, v5, v5
	v_mul_f32_e32 v5, 0xbfb8aa3b, v5
	v_exp_f32_e32 v5, v5
	v_mov_b32_e32 v11, v9
	v_add_f32_e32 v5, 1.0, v5
	v_rcp_f32_e32 v10, v5
	v_mul_f32_e32 v5, 0x3d372713, v9
	v_mul_f32_e32 v5, v5, v9
	v_fmac_f32_e32 v11, v5, v11
	v_mul_f32_e32 v5, 0x3f4c422a, v11
	v_add_f32_e32 v5, v5, v5
	v_mul_f32_e32 v5, 0xbfb8aa3b, v5
	v_exp_f32_e32 v5, v5
	s_nop 0
	v_add_f32_e32 v5, 1.0, v5
	v_rcp_f32_e32 v11, v5
	s_nop 0
	v_pk_mul_f32 v[8:9], v[10:11], v[8:9]
	s_nop 0
	v_pk_mul_f32 v[6:7], v[8:9], v[6:7]
	s_nop 0
	v_cvt_pk_bf16_f32 v5, v6, v7
	v_mad_i64_i32 v[6:7], s[8:9], v0, s13, v[72:73]
	v_or_b32_e32 v0, s4, v79
	global_store_dwordx4 v[6:7], v[2:5], off
	v_mad_i64_i32 v[6:7], s[8:9], v0, s13, v[74:75]
	ds_read_b128 v[2:5], v109 offset:288
	s_waitcnt lgkmcnt(0)
	v_lshlrev_b32_e32 v10, 16, v2
	v_and_b32_e32 v11, 0xffff0000, v2
	s_waitcnt vmcnt(7)
	v_mov_b32_e32 v6, v20
	v_mov_b32_e32 v7, v21
	v_mov_b32_e32 v8, v22
	v_mov_b32_e32 v9, v23
	v_lshlrev_b32_e32 v12, 16, v6
	v_mul_f32_e32 v2, 0x3d372713, v12
	v_and_b32_e32 v13, 0xffff0000, v6
	v_mul_f32_e32 v2, v2, v12
	v_mov_b32_e32 v6, v12
	v_fmac_f32_e32 v6, v2, v6
	v_mul_f32_e32 v2, 0x3f4c422a, v6
	v_add_f32_e32 v2, v2, v2
	v_mul_f32_e32 v2, 0xbfb8aa3b, v2
	v_exp_f32_e32 v2, v2
	v_mov_b32_e32 v6, v13
	v_add_f32_e32 v2, 1.0, v2
	v_rcp_f32_e32 v14, v2
	v_mul_f32_e32 v2, 0x3d372713, v13
	v_mul_f32_e32 v2, v2, v13
	v_fmac_f32_e32 v6, v2, v6
	v_mul_f32_e32 v2, 0x3f4c422a, v6
	v_add_f32_e32 v2, v2, v2
	v_mul_f32_e32 v2, 0xbfb8aa3b, v2
	v_exp_f32_e32 v2, v2
	v_lshlrev_b32_e32 v6, 16, v7
	v_and_b32_e32 v7, 0xffff0000, v7
	v_add_f32_e32 v2, 1.0, v2
	v_rcp_f32_e32 v15, v2
	s_nop 0
	v_pk_mul_f32 v[12:13], v[14:15], v[12:13]
	s_nop 0
	v_pk_mul_f32 v[10:11], v[12:13], v[10:11]
	v_mov_b32_e32 v12, v6
	v_cvt_pk_bf16_f32 v2, v10, v11
	v_lshlrev_b32_e32 v10, 16, v3
	v_and_b32_e32 v11, 0xffff0000, v3
	v_mul_f32_e32 v3, 0x3d372713, v6
	v_mul_f32_e32 v3, v3, v6
	v_fmac_f32_e32 v12, v3, v12
	v_mul_f32_e32 v3, 0x3f4c422a, v12
	v_add_f32_e32 v3, v3, v3
	v_mul_f32_e32 v3, 0xbfb8aa3b, v3
	v_exp_f32_e32 v3, v3
	v_mov_b32_e32 v13, v7
	v_add_f32_e32 v3, 1.0, v3
	v_rcp_f32_e32 v12, v3
	v_mul_f32_e32 v3, 0x3d372713, v7
	v_mul_f32_e32 v3, v3, v7
	v_fmac_f32_e32 v13, v3, v13
	v_mul_f32_e32 v3, 0x3f4c422a, v13
	v_add_f32_e32 v3, v3, v3
	v_mul_f32_e32 v3, 0xbfb8aa3b, v3
	v_exp_f32_e32 v3, v3
	s_nop 0
	v_add_f32_e32 v3, 1.0, v3
	v_rcp_f32_e32 v13, v3
	s_nop 0
	v_pk_mul_f32 v[6:7], v[12:13], v[6:7]
	s_nop 0
	v_pk_mul_f32 v[6:7], v[6:7], v[10:11]
	v_lshlrev_b32_e32 v10, 16, v8
	v_cvt_pk_bf16_f32 v3, v6, v7
	v_lshlrev_b32_e32 v6, 16, v4
	v_and_b32_e32 v7, 0xffff0000, v4
	v_mul_f32_e32 v4, 0x3d372713, v10
	v_and_b32_e32 v11, 0xffff0000, v8
	v_mul_f32_e32 v4, v4, v10
	v_mov_b32_e32 v8, v10
	v_fmac_f32_e32 v8, v4, v8
	v_mul_f32_e32 v4, 0x3f4c422a, v8
	v_add_f32_e32 v4, v4, v4
	v_mul_f32_e32 v4, 0xbfb8aa3b, v4
	v_exp_f32_e32 v4, v4
	v_mov_b32_e32 v8, v11
	v_add_f32_e32 v4, 1.0, v4
	v_rcp_f32_e32 v12, v4
	v_mul_f32_e32 v4, 0x3d372713, v11
	v_mul_f32_e32 v4, v4, v11
	v_fmac_f32_e32 v8, v4, v8
	v_mul_f32_e32 v4, 0x3f4c422a, v8
	v_add_f32_e32 v4, v4, v4
	v_mul_f32_e32 v4, 0xbfb8aa3b, v4
	v_exp_f32_e32 v4, v4
	v_lshlrev_b32_e32 v8, 16, v9
	v_and_b32_e32 v9, 0xffff0000, v9
	v_add_f32_e32 v4, 1.0, v4
	v_rcp_f32_e32 v13, v4
	s_nop 0
	v_pk_mul_f32 v[10:11], v[12:13], v[10:11]
	s_nop 0
	v_pk_mul_f32 v[6:7], v[10:11], v[6:7]
	v_mov_b32_e32 v10, v8
	v_cvt_pk_bf16_f32 v4, v6, v7
	v_lshlrev_b32_e32 v6, 16, v5
	v_and_b32_e32 v7, 0xffff0000, v5
	v_mul_f32_e32 v5, 0x3d372713, v8
	v_mul_f32_e32 v5, v5, v8
	v_fmac_f32_e32 v10, v5, v10
	v_mul_f32_e32 v5, 0x3f4c422a, v10
	v_add_f32_e32 v5, v5, v5
	v_mul_f32_e32 v5, 0xbfb8aa3b, v5
	v_exp_f32_e32 v5, v5
	v_mov_b32_e32 v11, v9
	v_add_f32_e32 v5, 1.0, v5
	v_rcp_f32_e32 v10, v5
	v_mul_f32_e32 v5, 0x3d372713, v9
	v_mul_f32_e32 v5, v5, v9
	v_fmac_f32_e32 v11, v5, v11
	v_mul_f32_e32 v5, 0x3f4c422a, v11
	v_add_f32_e32 v5, v5, v5
	v_mul_f32_e32 v5, 0xbfb8aa3b, v5
	v_exp_f32_e32 v5, v5
	s_nop 0
	v_add_f32_e32 v5, 1.0, v5
	v_rcp_f32_e32 v11, v5
	s_nop 0
	v_pk_mul_f32 v[8:9], v[10:11], v[8:9]
	s_nop 0
	v_pk_mul_f32 v[6:7], v[8:9], v[6:7]
	s_nop 0
	v_cvt_pk_bf16_f32 v5, v6, v7
	v_mad_i64_i32 v[6:7], s[8:9], v0, s13, v[72:73]
	v_or_b32_e32 v0, s4, v81
	global_store_dwordx4 v[6:7], v[2:5], off
	v_mad_i64_i32 v[6:7], s[8:9], v0, s13, v[74:75]
	ds_read_b128 v[2:5], v110 offset:288
	s_waitcnt lgkmcnt(0)
	v_lshlrev_b32_e32 v10, 16, v2
	v_and_b32_e32 v11, 0xffff0000, v2
	s_waitcnt vmcnt(7)
	v_mov_b32_e32 v6, v24
	v_mov_b32_e32 v7, v25
	v_mov_b32_e32 v8, v26
	v_mov_b32_e32 v9, v27
	v_lshlrev_b32_e32 v12, 16, v6
	v_mul_f32_e32 v2, 0x3d372713, v12
	v_and_b32_e32 v13, 0xffff0000, v6
	v_mul_f32_e32 v2, v2, v12
	v_mov_b32_e32 v6, v12
	v_fmac_f32_e32 v6, v2, v6
	v_mul_f32_e32 v2, 0x3f4c422a, v6
	v_add_f32_e32 v2, v2, v2
	v_mul_f32_e32 v2, 0xbfb8aa3b, v2
	v_exp_f32_e32 v2, v2
	v_mov_b32_e32 v6, v13
	v_add_f32_e32 v2, 1.0, v2
	v_rcp_f32_e32 v14, v2
	v_mul_f32_e32 v2, 0x3d372713, v13
	v_mul_f32_e32 v2, v2, v13
	v_fmac_f32_e32 v6, v2, v6
	v_mul_f32_e32 v2, 0x3f4c422a, v6
	v_add_f32_e32 v2, v2, v2
	v_mul_f32_e32 v2, 0xbfb8aa3b, v2
	v_exp_f32_e32 v2, v2
	v_lshlrev_b32_e32 v6, 16, v7
	v_and_b32_e32 v7, 0xffff0000, v7
	v_add_f32_e32 v2, 1.0, v2
	v_rcp_f32_e32 v15, v2
	s_nop 0
	v_pk_mul_f32 v[12:13], v[14:15], v[12:13]
	s_nop 0
	v_pk_mul_f32 v[10:11], v[12:13], v[10:11]
	v_mov_b32_e32 v12, v6
	v_cvt_pk_bf16_f32 v2, v10, v11
	v_lshlrev_b32_e32 v10, 16, v3
	v_and_b32_e32 v11, 0xffff0000, v3
	v_mul_f32_e32 v3, 0x3d372713, v6
	v_mul_f32_e32 v3, v3, v6
	v_fmac_f32_e32 v12, v3, v12
	v_mul_f32_e32 v3, 0x3f4c422a, v12
	v_add_f32_e32 v3, v3, v3
	v_mul_f32_e32 v3, 0xbfb8aa3b, v3
	v_exp_f32_e32 v3, v3
	v_mov_b32_e32 v13, v7
	v_add_f32_e32 v3, 1.0, v3
	v_rcp_f32_e32 v12, v3
	v_mul_f32_e32 v3, 0x3d372713, v7
	v_mul_f32_e32 v3, v3, v7
	v_fmac_f32_e32 v13, v3, v13
	v_mul_f32_e32 v3, 0x3f4c422a, v13
	v_add_f32_e32 v3, v3, v3
	v_mul_f32_e32 v3, 0xbfb8aa3b, v3
	v_exp_f32_e32 v3, v3
	s_nop 0
	v_add_f32_e32 v3, 1.0, v3
	v_rcp_f32_e32 v13, v3
	s_nop 0
	v_pk_mul_f32 v[6:7], v[12:13], v[6:7]
	s_nop 0
	v_pk_mul_f32 v[6:7], v[6:7], v[10:11]
	v_lshlrev_b32_e32 v10, 16, v8
	v_cvt_pk_bf16_f32 v3, v6, v7
	v_lshlrev_b32_e32 v6, 16, v4
	v_and_b32_e32 v7, 0xffff0000, v4
	v_mul_f32_e32 v4, 0x3d372713, v10
	v_and_b32_e32 v11, 0xffff0000, v8
	v_mul_f32_e32 v4, v4, v10
	v_mov_b32_e32 v8, v10
	v_fmac_f32_e32 v8, v4, v8
	v_mul_f32_e32 v4, 0x3f4c422a, v8
	v_add_f32_e32 v4, v4, v4
	v_mul_f32_e32 v4, 0xbfb8aa3b, v4
	v_exp_f32_e32 v4, v4
	v_mov_b32_e32 v8, v11
	v_add_f32_e32 v4, 1.0, v4
	v_rcp_f32_e32 v12, v4
	v_mul_f32_e32 v4, 0x3d372713, v11
	v_mul_f32_e32 v4, v4, v11
	v_fmac_f32_e32 v8, v4, v8
	v_mul_f32_e32 v4, 0x3f4c422a, v8
	v_add_f32_e32 v4, v4, v4
	v_mul_f32_e32 v4, 0xbfb8aa3b, v4
	v_exp_f32_e32 v4, v4
	v_lshlrev_b32_e32 v8, 16, v9
	v_and_b32_e32 v9, 0xffff0000, v9
	v_add_f32_e32 v4, 1.0, v4
	v_rcp_f32_e32 v13, v4
	s_nop 0
	v_pk_mul_f32 v[10:11], v[12:13], v[10:11]
	s_nop 0
	v_pk_mul_f32 v[6:7], v[10:11], v[6:7]
	v_mov_b32_e32 v10, v8
	v_cvt_pk_bf16_f32 v4, v6, v7
	v_lshlrev_b32_e32 v6, 16, v5
	v_and_b32_e32 v7, 0xffff0000, v5
	v_mul_f32_e32 v5, 0x3d372713, v8
	v_mul_f32_e32 v5, v5, v8
	v_fmac_f32_e32 v10, v5, v10
	v_mul_f32_e32 v5, 0x3f4c422a, v10
	v_add_f32_e32 v5, v5, v5
	v_mul_f32_e32 v5, 0xbfb8aa3b, v5
	v_exp_f32_e32 v5, v5
	v_mov_b32_e32 v11, v9
	v_add_f32_e32 v5, 1.0, v5
	v_rcp_f32_e32 v10, v5
	v_mul_f32_e32 v5, 0x3d372713, v9
	v_mul_f32_e32 v5, v5, v9
	v_fmac_f32_e32 v11, v5, v11
	v_mul_f32_e32 v5, 0x3f4c422a, v11
	v_add_f32_e32 v5, v5, v5
	v_mul_f32_e32 v5, 0xbfb8aa3b, v5
	v_exp_f32_e32 v5, v5
	s_nop 0
	v_add_f32_e32 v5, 1.0, v5
	v_rcp_f32_e32 v11, v5
	s_nop 0
	v_pk_mul_f32 v[8:9], v[10:11], v[8:9]
	s_nop 0
	v_pk_mul_f32 v[6:7], v[8:9], v[6:7]
	s_nop 0
	v_cvt_pk_bf16_f32 v5, v6, v7
	v_mad_i64_i32 v[6:7], s[8:9], v0, s13, v[72:73]
	v_or_b32_e32 v0, s4, v83
	global_store_dwordx4 v[6:7], v[2:5], off
	v_mad_i64_i32 v[6:7], s[8:9], v0, s13, v[74:75]
	ds_read_b128 v[2:5], v111 offset:288
	s_waitcnt lgkmcnt(0)
	v_lshlrev_b32_e32 v10, 16, v2
	v_and_b32_e32 v11, 0xffff0000, v2
	s_waitcnt vmcnt(7)
	v_mov_b32_e32 v6, v28
	v_mov_b32_e32 v7, v29
	v_mov_b32_e32 v8, v30
	v_mov_b32_e32 v9, v31
	v_lshlrev_b32_e32 v12, 16, v6
	v_mul_f32_e32 v2, 0x3d372713, v12
	v_and_b32_e32 v13, 0xffff0000, v6
	v_mul_f32_e32 v2, v2, v12
	v_mov_b32_e32 v6, v12
	v_fmac_f32_e32 v6, v2, v6
	v_mul_f32_e32 v2, 0x3f4c422a, v6
	v_add_f32_e32 v2, v2, v2
	v_mul_f32_e32 v2, 0xbfb8aa3b, v2
	v_exp_f32_e32 v2, v2
	v_mov_b32_e32 v6, v13
	v_add_f32_e32 v2, 1.0, v2
	v_rcp_f32_e32 v14, v2
	v_mul_f32_e32 v2, 0x3d372713, v13
	v_mul_f32_e32 v2, v2, v13
	v_fmac_f32_e32 v6, v2, v6
	v_mul_f32_e32 v2, 0x3f4c422a, v6
	v_add_f32_e32 v2, v2, v2
	v_mul_f32_e32 v2, 0xbfb8aa3b, v2
	v_exp_f32_e32 v2, v2
	v_lshlrev_b32_e32 v6, 16, v7
	v_and_b32_e32 v7, 0xffff0000, v7
	v_add_f32_e32 v2, 1.0, v2
	v_rcp_f32_e32 v15, v2
	s_nop 0
	v_pk_mul_f32 v[12:13], v[14:15], v[12:13]
	s_nop 0
	v_pk_mul_f32 v[10:11], v[12:13], v[10:11]
	v_mov_b32_e32 v12, v6
	v_cvt_pk_bf16_f32 v2, v10, v11
	v_lshlrev_b32_e32 v10, 16, v3
	v_and_b32_e32 v11, 0xffff0000, v3
	v_mul_f32_e32 v3, 0x3d372713, v6
	v_mul_f32_e32 v3, v3, v6
	v_fmac_f32_e32 v12, v3, v12
	v_mul_f32_e32 v3, 0x3f4c422a, v12
	v_add_f32_e32 v3, v3, v3
	v_mul_f32_e32 v3, 0xbfb8aa3b, v3
	v_exp_f32_e32 v3, v3
	v_mov_b32_e32 v13, v7
	v_add_f32_e32 v3, 1.0, v3
	v_rcp_f32_e32 v12, v3
	v_mul_f32_e32 v3, 0x3d372713, v7
	v_mul_f32_e32 v3, v3, v7
	v_fmac_f32_e32 v13, v3, v13
	v_mul_f32_e32 v3, 0x3f4c422a, v13
	v_add_f32_e32 v3, v3, v3
	v_mul_f32_e32 v3, 0xbfb8aa3b, v3
	v_exp_f32_e32 v3, v3
	s_nop 0
	v_add_f32_e32 v3, 1.0, v3
	v_rcp_f32_e32 v13, v3
	s_nop 0
	v_pk_mul_f32 v[6:7], v[12:13], v[6:7]
	s_nop 0
	v_pk_mul_f32 v[6:7], v[6:7], v[10:11]
	v_lshlrev_b32_e32 v10, 16, v8
	v_cvt_pk_bf16_f32 v3, v6, v7
	v_lshlrev_b32_e32 v6, 16, v4
	v_and_b32_e32 v7, 0xffff0000, v4
	v_mul_f32_e32 v4, 0x3d372713, v10
	v_and_b32_e32 v11, 0xffff0000, v8
	v_mul_f32_e32 v4, v4, v10
	v_mov_b32_e32 v8, v10
	v_fmac_f32_e32 v8, v4, v8
	v_mul_f32_e32 v4, 0x3f4c422a, v8
	v_add_f32_e32 v4, v4, v4
	v_mul_f32_e32 v4, 0xbfb8aa3b, v4
	v_exp_f32_e32 v4, v4
	v_mov_b32_e32 v8, v11
	v_add_f32_e32 v4, 1.0, v4
	v_rcp_f32_e32 v12, v4
	v_mul_f32_e32 v4, 0x3d372713, v11
	v_mul_f32_e32 v4, v4, v11
	v_fmac_f32_e32 v8, v4, v8
	v_mul_f32_e32 v4, 0x3f4c422a, v8
	v_add_f32_e32 v4, v4, v4
	v_mul_f32_e32 v4, 0xbfb8aa3b, v4
	v_exp_f32_e32 v4, v4
	v_lshlrev_b32_e32 v8, 16, v9
	v_and_b32_e32 v9, 0xffff0000, v9
	v_add_f32_e32 v4, 1.0, v4
	v_rcp_f32_e32 v13, v4
	s_nop 0
	v_pk_mul_f32 v[10:11], v[12:13], v[10:11]
	s_nop 0
	v_pk_mul_f32 v[6:7], v[10:11], v[6:7]
	v_mov_b32_e32 v10, v8
	v_cvt_pk_bf16_f32 v4, v6, v7
	v_lshlrev_b32_e32 v6, 16, v5
	v_and_b32_e32 v7, 0xffff0000, v5
	v_mul_f32_e32 v5, 0x3d372713, v8
	v_mul_f32_e32 v5, v5, v8
	v_fmac_f32_e32 v10, v5, v10
	v_mul_f32_e32 v5, 0x3f4c422a, v10
	v_add_f32_e32 v5, v5, v5
	v_mul_f32_e32 v5, 0xbfb8aa3b, v5
	v_exp_f32_e32 v5, v5
	v_mov_b32_e32 v11, v9
	v_add_f32_e32 v5, 1.0, v5
	v_rcp_f32_e32 v10, v5
	v_mul_f32_e32 v5, 0x3d372713, v9
	v_mul_f32_e32 v5, v5, v9
	v_fmac_f32_e32 v11, v5, v11
	v_mul_f32_e32 v5, 0x3f4c422a, v11
	v_add_f32_e32 v5, v5, v5
	v_mul_f32_e32 v5, 0xbfb8aa3b, v5
	v_exp_f32_e32 v5, v5
	s_nop 0
	v_add_f32_e32 v5, 1.0, v5
	v_rcp_f32_e32 v11, v5
	s_nop 0
	v_pk_mul_f32 v[8:9], v[10:11], v[8:9]
	s_nop 0
	v_pk_mul_f32 v[6:7], v[8:9], v[6:7]
	s_nop 0
	v_cvt_pk_bf16_f32 v5, v6, v7
	v_mad_i64_i32 v[6:7], s[8:9], v0, s13, v[72:73]
	v_or_b32_e32 v0, s4, v85
	global_store_dwordx4 v[6:7], v[2:5], off
	v_mad_i64_i32 v[6:7], s[8:9], v0, s13, v[74:75]
	ds_read_b128 v[2:5], v112 offset:288
	s_waitcnt lgkmcnt(0)
	v_lshlrev_b32_e32 v10, 16, v2
	v_and_b32_e32 v11, 0xffff0000, v2
	s_waitcnt vmcnt(7)
	v_mov_b32_e32 v6, v32
	v_mov_b32_e32 v7, v33
	v_mov_b32_e32 v8, v34
	v_mov_b32_e32 v9, v35
	v_lshlrev_b32_e32 v12, 16, v6
	v_mul_f32_e32 v2, 0x3d372713, v12
	v_and_b32_e32 v13, 0xffff0000, v6
	v_mul_f32_e32 v2, v2, v12
	v_mov_b32_e32 v6, v12
	v_fmac_f32_e32 v6, v2, v6
	v_mul_f32_e32 v2, 0x3f4c422a, v6
	v_add_f32_e32 v2, v2, v2
	v_mul_f32_e32 v2, 0xbfb8aa3b, v2
	v_exp_f32_e32 v2, v2
	v_mov_b32_e32 v6, v13
	v_add_f32_e32 v2, 1.0, v2
	v_rcp_f32_e32 v14, v2
	v_mul_f32_e32 v2, 0x3d372713, v13
	v_mul_f32_e32 v2, v2, v13
	v_fmac_f32_e32 v6, v2, v6
	v_mul_f32_e32 v2, 0x3f4c422a, v6
	v_add_f32_e32 v2, v2, v2
	v_mul_f32_e32 v2, 0xbfb8aa3b, v2
	v_exp_f32_e32 v2, v2
	v_lshlrev_b32_e32 v6, 16, v7
	v_and_b32_e32 v7, 0xffff0000, v7
	v_add_f32_e32 v2, 1.0, v2
	v_rcp_f32_e32 v15, v2
	s_nop 0
	v_pk_mul_f32 v[12:13], v[14:15], v[12:13]
	s_nop 0
	v_pk_mul_f32 v[10:11], v[12:13], v[10:11]
	v_mov_b32_e32 v12, v6
	v_cvt_pk_bf16_f32 v2, v10, v11
	v_lshlrev_b32_e32 v10, 16, v3
	v_and_b32_e32 v11, 0xffff0000, v3
	v_mul_f32_e32 v3, 0x3d372713, v6
	v_mul_f32_e32 v3, v3, v6
	v_fmac_f32_e32 v12, v3, v12
	v_mul_f32_e32 v3, 0x3f4c422a, v12
	v_add_f32_e32 v3, v3, v3
	v_mul_f32_e32 v3, 0xbfb8aa3b, v3
	v_exp_f32_e32 v3, v3
	v_mov_b32_e32 v13, v7
	v_add_f32_e32 v3, 1.0, v3
	v_rcp_f32_e32 v12, v3
	v_mul_f32_e32 v3, 0x3d372713, v7
	v_mul_f32_e32 v3, v3, v7
	v_fmac_f32_e32 v13, v3, v13
	v_mul_f32_e32 v3, 0x3f4c422a, v13
	v_add_f32_e32 v3, v3, v3
	v_mul_f32_e32 v3, 0xbfb8aa3b, v3
	v_exp_f32_e32 v3, v3
	s_nop 0
	v_add_f32_e32 v3, 1.0, v3
	v_rcp_f32_e32 v13, v3
	s_nop 0
	v_pk_mul_f32 v[6:7], v[12:13], v[6:7]
	s_nop 0
	v_pk_mul_f32 v[6:7], v[6:7], v[10:11]
	v_lshlrev_b32_e32 v10, 16, v8
	v_cvt_pk_bf16_f32 v3, v6, v7
	v_lshlrev_b32_e32 v6, 16, v4
	v_and_b32_e32 v7, 0xffff0000, v4
	v_mul_f32_e32 v4, 0x3d372713, v10
	v_and_b32_e32 v11, 0xffff0000, v8
	v_mul_f32_e32 v4, v4, v10
	v_mov_b32_e32 v8, v10
	v_fmac_f32_e32 v8, v4, v8
	v_mul_f32_e32 v4, 0x3f4c422a, v8
	v_add_f32_e32 v4, v4, v4
	v_mul_f32_e32 v4, 0xbfb8aa3b, v4
	v_exp_f32_e32 v4, v4
	v_mov_b32_e32 v8, v11
	v_add_f32_e32 v4, 1.0, v4
	v_rcp_f32_e32 v12, v4
	v_mul_f32_e32 v4, 0x3d372713, v11
	v_mul_f32_e32 v4, v4, v11
	v_fmac_f32_e32 v8, v4, v8
	v_mul_f32_e32 v4, 0x3f4c422a, v8
	v_add_f32_e32 v4, v4, v4
	v_mul_f32_e32 v4, 0xbfb8aa3b, v4
	v_exp_f32_e32 v4, v4
	v_lshlrev_b32_e32 v8, 16, v9
	v_and_b32_e32 v9, 0xffff0000, v9
	v_add_f32_e32 v4, 1.0, v4
	v_rcp_f32_e32 v13, v4
	s_nop 0
	v_pk_mul_f32 v[10:11], v[12:13], v[10:11]
	s_nop 0
	v_pk_mul_f32 v[6:7], v[10:11], v[6:7]
	v_mov_b32_e32 v10, v8
	v_cvt_pk_bf16_f32 v4, v6, v7
	v_lshlrev_b32_e32 v6, 16, v5
	v_and_b32_e32 v7, 0xffff0000, v5
	v_mul_f32_e32 v5, 0x3d372713, v8
	v_mul_f32_e32 v5, v5, v8
	v_fmac_f32_e32 v10, v5, v10
	v_mul_f32_e32 v5, 0x3f4c422a, v10
	v_add_f32_e32 v5, v5, v5
	v_mul_f32_e32 v5, 0xbfb8aa3b, v5
	v_exp_f32_e32 v5, v5
	v_mov_b32_e32 v11, v9
	v_add_f32_e32 v5, 1.0, v5
	v_rcp_f32_e32 v10, v5
	v_mul_f32_e32 v5, 0x3d372713, v9
	v_mul_f32_e32 v5, v5, v9
	v_fmac_f32_e32 v11, v5, v11
	v_mul_f32_e32 v5, 0x3f4c422a, v11
	v_add_f32_e32 v5, v5, v5
	v_mul_f32_e32 v5, 0xbfb8aa3b, v5
	v_exp_f32_e32 v5, v5
	s_nop 0
	v_add_f32_e32 v5, 1.0, v5
	v_rcp_f32_e32 v11, v5
	s_nop 0
	v_pk_mul_f32 v[8:9], v[10:11], v[8:9]
	s_nop 0
	v_pk_mul_f32 v[6:7], v[8:9], v[6:7]
	s_nop 0
	v_cvt_pk_bf16_f32 v5, v6, v7
	v_mad_i64_i32 v[6:7], s[8:9], v0, s13, v[72:73]
	v_or_b32_e32 v0, s4, v87
	global_store_dwordx4 v[6:7], v[2:5], off
	v_mad_i64_i32 v[6:7], s[8:9], v0, s13, v[74:75]
	ds_read_b128 v[2:5], v113 offset:288
	s_waitcnt lgkmcnt(0)
	v_lshlrev_b32_e32 v10, 16, v2
	v_and_b32_e32 v11, 0xffff0000, v2
	s_waitcnt vmcnt(7)
	v_mov_b32_e32 v6, v36
	v_mov_b32_e32 v7, v37
	v_mov_b32_e32 v8, v38
	v_mov_b32_e32 v9, v39
	v_lshlrev_b32_e32 v12, 16, v6
	v_mul_f32_e32 v2, 0x3d372713, v12
	v_and_b32_e32 v13, 0xffff0000, v6
	v_mul_f32_e32 v2, v2, v12
	v_mov_b32_e32 v6, v12
	v_fmac_f32_e32 v6, v2, v6
	v_mul_f32_e32 v2, 0x3f4c422a, v6
	v_add_f32_e32 v2, v2, v2
	v_mul_f32_e32 v2, 0xbfb8aa3b, v2
	v_exp_f32_e32 v2, v2
	v_mov_b32_e32 v6, v13
	v_add_f32_e32 v2, 1.0, v2
	v_rcp_f32_e32 v14, v2
	v_mul_f32_e32 v2, 0x3d372713, v13
	v_mul_f32_e32 v2, v2, v13
	v_fmac_f32_e32 v6, v2, v6
	v_mul_f32_e32 v2, 0x3f4c422a, v6
	v_add_f32_e32 v2, v2, v2
	v_mul_f32_e32 v2, 0xbfb8aa3b, v2
	v_exp_f32_e32 v2, v2
	v_lshlrev_b32_e32 v6, 16, v7
	v_and_b32_e32 v7, 0xffff0000, v7
	v_add_f32_e32 v2, 1.0, v2
	v_rcp_f32_e32 v15, v2
	s_nop 0
	v_pk_mul_f32 v[12:13], v[14:15], v[12:13]
	s_nop 0
	v_pk_mul_f32 v[10:11], v[12:13], v[10:11]
	v_mov_b32_e32 v12, v6
	v_cvt_pk_bf16_f32 v2, v10, v11
	v_lshlrev_b32_e32 v10, 16, v3
	v_and_b32_e32 v11, 0xffff0000, v3
	v_mul_f32_e32 v3, 0x3d372713, v6
	v_mul_f32_e32 v3, v3, v6
	v_fmac_f32_e32 v12, v3, v12
	v_mul_f32_e32 v3, 0x3f4c422a, v12
	v_add_f32_e32 v3, v3, v3
	v_mul_f32_e32 v3, 0xbfb8aa3b, v3
	v_exp_f32_e32 v3, v3
	v_mov_b32_e32 v13, v7
	v_add_f32_e32 v3, 1.0, v3
	v_rcp_f32_e32 v12, v3
	v_mul_f32_e32 v3, 0x3d372713, v7
	v_mul_f32_e32 v3, v3, v7
	v_fmac_f32_e32 v13, v3, v13
	v_mul_f32_e32 v3, 0x3f4c422a, v13
	v_add_f32_e32 v3, v3, v3
	v_mul_f32_e32 v3, 0xbfb8aa3b, v3
	v_exp_f32_e32 v3, v3
	s_nop 0
	v_add_f32_e32 v3, 1.0, v3
	v_rcp_f32_e32 v13, v3
	s_nop 0
	v_pk_mul_f32 v[6:7], v[12:13], v[6:7]
	s_nop 0
	v_pk_mul_f32 v[6:7], v[6:7], v[10:11]
	v_lshlrev_b32_e32 v10, 16, v8
	v_cvt_pk_bf16_f32 v3, v6, v7
	v_lshlrev_b32_e32 v6, 16, v4
	v_and_b32_e32 v7, 0xffff0000, v4
	v_mul_f32_e32 v4, 0x3d372713, v10
	v_and_b32_e32 v11, 0xffff0000, v8
	v_mul_f32_e32 v4, v4, v10
	v_mov_b32_e32 v8, v10
	v_fmac_f32_e32 v8, v4, v8
	v_mul_f32_e32 v4, 0x3f4c422a, v8
	v_add_f32_e32 v4, v4, v4
	v_mul_f32_e32 v4, 0xbfb8aa3b, v4
	v_exp_f32_e32 v4, v4
	v_mov_b32_e32 v8, v11
	v_add_f32_e32 v4, 1.0, v4
	v_rcp_f32_e32 v12, v4
	v_mul_f32_e32 v4, 0x3d372713, v11
	v_mul_f32_e32 v4, v4, v11
	v_fmac_f32_e32 v8, v4, v8
	v_mul_f32_e32 v4, 0x3f4c422a, v8
	v_add_f32_e32 v4, v4, v4
	v_mul_f32_e32 v4, 0xbfb8aa3b, v4
	v_exp_f32_e32 v4, v4
	v_lshlrev_b32_e32 v8, 16, v9
	v_and_b32_e32 v9, 0xffff0000, v9
	v_add_f32_e32 v4, 1.0, v4
	v_rcp_f32_e32 v13, v4
	s_nop 0
	v_pk_mul_f32 v[10:11], v[12:13], v[10:11]
	s_nop 0
	v_pk_mul_f32 v[6:7], v[10:11], v[6:7]
	v_mov_b32_e32 v10, v8
	v_cvt_pk_bf16_f32 v4, v6, v7
	v_lshlrev_b32_e32 v6, 16, v5
	v_and_b32_e32 v7, 0xffff0000, v5
	v_mul_f32_e32 v5, 0x3d372713, v8
	v_mul_f32_e32 v5, v5, v8
	v_fmac_f32_e32 v10, v5, v10
	v_mul_f32_e32 v5, 0x3f4c422a, v10
	v_add_f32_e32 v5, v5, v5
	v_mul_f32_e32 v5, 0xbfb8aa3b, v5
	v_exp_f32_e32 v5, v5
	v_mov_b32_e32 v11, v9
	v_add_f32_e32 v5, 1.0, v5
	v_rcp_f32_e32 v10, v5
	v_mul_f32_e32 v5, 0x3d372713, v9
	v_mul_f32_e32 v5, v5, v9
	v_fmac_f32_e32 v11, v5, v11
	v_mul_f32_e32 v5, 0x3f4c422a, v11
	v_add_f32_e32 v5, v5, v5
	v_mul_f32_e32 v5, 0xbfb8aa3b, v5
	v_exp_f32_e32 v5, v5
	s_nop 0
	v_add_f32_e32 v5, 1.0, v5
	v_rcp_f32_e32 v11, v5
	s_nop 0
	v_pk_mul_f32 v[8:9], v[10:11], v[8:9]
	s_nop 0
	v_pk_mul_f32 v[6:7], v[8:9], v[6:7]
	s_nop 0
	v_cvt_pk_bf16_f32 v5, v6, v7
	v_mad_i64_i32 v[6:7], s[8:9], v0, s13, v[72:73]
	v_or_b32_e32 v0, s4, v89
	global_store_dwordx4 v[6:7], v[2:5], off
	v_mad_i64_i32 v[6:7], s[8:9], v0, s13, v[74:75]
	ds_read_b128 v[2:5], v114 offset:288
	s_waitcnt lgkmcnt(0)
	v_lshlrev_b32_e32 v10, 16, v2
	v_and_b32_e32 v11, 0xffff0000, v2
	s_waitcnt vmcnt(7)
	v_mov_b32_e32 v6, v40
	v_mov_b32_e32 v7, v41
	v_mov_b32_e32 v8, v42
	v_mov_b32_e32 v9, v43
	v_lshlrev_b32_e32 v12, 16, v6
	v_mul_f32_e32 v2, 0x3d372713, v12
	v_and_b32_e32 v13, 0xffff0000, v6
	v_mul_f32_e32 v2, v2, v12
	v_mov_b32_e32 v6, v12
	v_fmac_f32_e32 v6, v2, v6
	v_mul_f32_e32 v2, 0x3f4c422a, v6
	v_add_f32_e32 v2, v2, v2
	v_mul_f32_e32 v2, 0xbfb8aa3b, v2
	v_exp_f32_e32 v2, v2
	v_mov_b32_e32 v6, v13
	v_add_f32_e32 v2, 1.0, v2
	v_rcp_f32_e32 v14, v2
	v_mul_f32_e32 v2, 0x3d372713, v13
	v_mul_f32_e32 v2, v2, v13
	v_fmac_f32_e32 v6, v2, v6
	v_mul_f32_e32 v2, 0x3f4c422a, v6
	v_add_f32_e32 v2, v2, v2
	v_mul_f32_e32 v2, 0xbfb8aa3b, v2
	v_exp_f32_e32 v2, v2
	v_lshlrev_b32_e32 v6, 16, v7
	v_and_b32_e32 v7, 0xffff0000, v7
	v_add_f32_e32 v2, 1.0, v2
	v_rcp_f32_e32 v15, v2
	s_nop 0
	v_pk_mul_f32 v[12:13], v[14:15], v[12:13]
	s_nop 0
	v_pk_mul_f32 v[10:11], v[12:13], v[10:11]
	v_mov_b32_e32 v12, v6
	v_cvt_pk_bf16_f32 v2, v10, v11
	v_lshlrev_b32_e32 v10, 16, v3
	v_and_b32_e32 v11, 0xffff0000, v3
	v_mul_f32_e32 v3, 0x3d372713, v6
	v_mul_f32_e32 v3, v3, v6
	v_fmac_f32_e32 v12, v3, v12
	v_mul_f32_e32 v3, 0x3f4c422a, v12
	v_add_f32_e32 v3, v3, v3
	v_mul_f32_e32 v3, 0xbfb8aa3b, v3
	v_exp_f32_e32 v3, v3
	v_mov_b32_e32 v13, v7
	v_add_f32_e32 v3, 1.0, v3
	v_rcp_f32_e32 v12, v3
	v_mul_f32_e32 v3, 0x3d372713, v7
	v_mul_f32_e32 v3, v3, v7
	v_fmac_f32_e32 v13, v3, v13
	v_mul_f32_e32 v3, 0x3f4c422a, v13
	v_add_f32_e32 v3, v3, v3
	v_mul_f32_e32 v3, 0xbfb8aa3b, v3
	v_exp_f32_e32 v3, v3
	s_nop 0
	v_add_f32_e32 v3, 1.0, v3
	v_rcp_f32_e32 v13, v3
	s_nop 0
	v_pk_mul_f32 v[6:7], v[12:13], v[6:7]
	s_nop 0
	v_pk_mul_f32 v[6:7], v[6:7], v[10:11]
	v_lshlrev_b32_e32 v10, 16, v8
	v_cvt_pk_bf16_f32 v3, v6, v7
	v_lshlrev_b32_e32 v6, 16, v4
	v_and_b32_e32 v7, 0xffff0000, v4
	v_mul_f32_e32 v4, 0x3d372713, v10
	v_and_b32_e32 v11, 0xffff0000, v8
	v_mul_f32_e32 v4, v4, v10
	v_mov_b32_e32 v8, v10
	v_fmac_f32_e32 v8, v4, v8
	v_mul_f32_e32 v4, 0x3f4c422a, v8
	v_add_f32_e32 v4, v4, v4
	v_mul_f32_e32 v4, 0xbfb8aa3b, v4
	v_exp_f32_e32 v4, v4
	v_mov_b32_e32 v8, v11
	v_add_f32_e32 v4, 1.0, v4
	v_rcp_f32_e32 v12, v4
	v_mul_f32_e32 v4, 0x3d372713, v11
	v_mul_f32_e32 v4, v4, v11
	v_fmac_f32_e32 v8, v4, v8
	v_mul_f32_e32 v4, 0x3f4c422a, v8
	v_add_f32_e32 v4, v4, v4
	v_mul_f32_e32 v4, 0xbfb8aa3b, v4
	v_exp_f32_e32 v4, v4
	v_lshlrev_b32_e32 v8, 16, v9
	v_and_b32_e32 v9, 0xffff0000, v9
	v_add_f32_e32 v4, 1.0, v4
	v_rcp_f32_e32 v13, v4
	s_nop 0
	v_pk_mul_f32 v[10:11], v[12:13], v[10:11]
	s_nop 0
	v_pk_mul_f32 v[6:7], v[10:11], v[6:7]
	v_mov_b32_e32 v10, v8
	v_cvt_pk_bf16_f32 v4, v6, v7
	v_lshlrev_b32_e32 v6, 16, v5
	v_and_b32_e32 v7, 0xffff0000, v5
	v_mul_f32_e32 v5, 0x3d372713, v8
	v_mul_f32_e32 v5, v5, v8
	v_fmac_f32_e32 v10, v5, v10
	v_mul_f32_e32 v5, 0x3f4c422a, v10
	v_add_f32_e32 v5, v5, v5
	v_mul_f32_e32 v5, 0xbfb8aa3b, v5
	v_exp_f32_e32 v5, v5
	v_mov_b32_e32 v11, v9
	v_add_f32_e32 v5, 1.0, v5
	v_rcp_f32_e32 v10, v5
	v_mul_f32_e32 v5, 0x3d372713, v9
	v_mul_f32_e32 v5, v5, v9
	v_fmac_f32_e32 v11, v5, v11
	v_mul_f32_e32 v5, 0x3f4c422a, v11
	v_add_f32_e32 v5, v5, v5
	v_mul_f32_e32 v5, 0xbfb8aa3b, v5
	v_exp_f32_e32 v5, v5
	s_nop 0
	v_add_f32_e32 v5, 1.0, v5
	v_rcp_f32_e32 v11, v5
	s_nop 0
	v_pk_mul_f32 v[8:9], v[10:11], v[8:9]
	s_nop 0
	v_pk_mul_f32 v[6:7], v[8:9], v[6:7]
	s_nop 0
	v_cvt_pk_bf16_f32 v5, v6, v7
	v_mad_i64_i32 v[6:7], s[8:9], v0, s13, v[72:73]
	v_or_b32_e32 v0, s4, v91
	global_store_dwordx4 v[6:7], v[2:5], off
	ds_read_b128 v[6:9], v115 offset:288
	s_waitcnt lgkmcnt(0)
	v_lshlrev_b32_e32 v10, 16, v6
	v_mad_i64_i32 v[2:3], s[4:5], v0, s13, v[74:75]
	v_and_b32_e32 v11, 0xffff0000, v6
	s_waitcnt vmcnt(7)
	v_mov_b32_e32 v2, v44
	v_mov_b32_e32 v3, v45
	v_mov_b32_e32 v4, v46
	v_mov_b32_e32 v5, v47
	v_lshlrev_b32_e32 v12, 16, v2
	v_and_b32_e32 v13, 0xffff0000, v2
	v_mul_f32_e32 v2, 0x3d372713, v12
	v_mul_f32_e32 v2, v2, v12
	v_mov_b32_e32 v6, v12
	v_fmac_f32_e32 v6, v2, v6
	v_mul_f32_e32 v2, 0x3f4c422a, v6
	v_add_f32_e32 v2, v2, v2
	v_mul_f32_e32 v2, 0xbfb8aa3b, v2
	v_exp_f32_e32 v2, v2
	v_mov_b32_e32 v6, v13
	v_add_f32_e32 v2, 1.0, v2
	v_rcp_f32_e32 v14, v2
	v_mul_f32_e32 v2, 0x3d372713, v13
	v_mul_f32_e32 v2, v2, v13
	v_fmac_f32_e32 v6, v2, v6
	v_mul_f32_e32 v2, 0x3f4c422a, v6
	v_add_f32_e32 v2, v2, v2
	v_mul_f32_e32 v2, 0xbfb8aa3b, v2
	v_exp_f32_e32 v2, v2
	v_lshlrev_b32_e32 v6, 16, v7
	v_and_b32_e32 v7, 0xffff0000, v7
	v_add_f32_e32 v2, 1.0, v2
	v_rcp_f32_e32 v15, v2
	s_nop 0
	v_pk_mul_f32 v[12:13], v[14:15], v[12:13]
	s_nop 0
	v_pk_mul_f32 v[10:11], v[12:13], v[10:11]
	s_nop 0
	v_cvt_pk_bf16_f32 v2, v10, v11
	v_lshlrev_b32_e32 v10, 16, v3
	v_and_b32_e32 v11, 0xffff0000, v3
	v_mul_f32_e32 v3, 0x3d372713, v10
	v_mul_f32_e32 v3, v3, v10
	v_mov_b32_e32 v12, v10
	v_fmac_f32_e32 v12, v3, v12
	v_mul_f32_e32 v3, 0x3f4c422a, v12
	v_add_f32_e32 v3, v3, v3
	v_mul_f32_e32 v3, 0xbfb8aa3b, v3
	v_exp_f32_e32 v3, v3
	v_mov_b32_e32 v13, v11
	v_add_f32_e32 v3, 1.0, v3
	v_rcp_f32_e32 v12, v3
	v_mul_f32_e32 v3, 0x3d372713, v11
	v_mul_f32_e32 v3, v3, v11
	v_fmac_f32_e32 v13, v3, v13
	v_mul_f32_e32 v3, 0x3f4c422a, v13
	v_add_f32_e32 v3, v3, v3
	v_mul_f32_e32 v3, 0xbfb8aa3b, v3
	v_exp_f32_e32 v3, v3
	s_nop 0
	v_add_f32_e32 v3, 1.0, v3
	v_rcp_f32_e32 v13, v3
	s_nop 0
	v_pk_mul_f32 v[10:11], v[12:13], v[10:11]
	s_nop 0
	v_pk_mul_f32 v[6:7], v[10:11], v[6:7]
	v_lshlrev_b32_e32 v10, 16, v4
	v_and_b32_e32 v11, 0xffff0000, v4
	v_mul_f32_e32 v4, 0x3d372713, v10
	v_cvt_pk_bf16_f32 v3, v6, v7
	v_lshlrev_b32_e32 v6, 16, v8
	v_and_b32_e32 v7, 0xffff0000, v8
	v_mul_f32_e32 v4, v4, v10
	v_mov_b32_e32 v8, v10
	v_fmac_f32_e32 v8, v4, v8
	v_mul_f32_e32 v4, 0x3f4c422a, v8
	v_add_f32_e32 v4, v4, v4
	v_mul_f32_e32 v4, 0xbfb8aa3b, v4
	v_exp_f32_e32 v4, v4
	v_mov_b32_e32 v8, v11
	v_add_f32_e32 v4, 1.0, v4
	v_rcp_f32_e32 v12, v4
	v_mul_f32_e32 v4, 0x3d372713, v11
	v_mul_f32_e32 v4, v4, v11
	v_fmac_f32_e32 v8, v4, v8
	v_mul_f32_e32 v4, 0x3f4c422a, v8
	v_add_f32_e32 v4, v4, v4
	v_mul_f32_e32 v4, 0xbfb8aa3b, v4
	v_exp_f32_e32 v4, v4
	v_lshlrev_b32_e32 v8, 16, v5
	v_add_f32_e32 v4, 1.0, v4
	v_rcp_f32_e32 v13, v4
	s_nop 0
	v_pk_mul_f32 v[10:11], v[12:13], v[10:11]
	s_nop 0
	v_pk_mul_f32 v[6:7], v[10:11], v[6:7]
	v_mov_b32_e32 v10, v8
	v_cvt_pk_bf16_f32 v4, v6, v7
	v_lshlrev_b32_e32 v6, 16, v9
	v_and_b32_e32 v7, 0xffff0000, v9
	v_and_b32_e32 v9, 0xffff0000, v5
	v_mul_f32_e32 v5, 0x3d372713, v8
	v_mul_f32_e32 v5, v5, v8
	v_fmac_f32_e32 v10, v5, v10
	v_mul_f32_e32 v5, 0x3f4c422a, v10
	v_add_f32_e32 v5, v5, v5
	v_mul_f32_e32 v5, 0xbfb8aa3b, v5
	v_exp_f32_e32 v5, v5
	v_mov_b32_e32 v11, v9
	v_add_f32_e32 v5, 1.0, v5
	v_rcp_f32_e32 v10, v5
	v_mul_f32_e32 v5, 0x3d372713, v9
	v_mul_f32_e32 v5, v5, v9
	v_fmac_f32_e32 v11, v5, v11
	v_mul_f32_e32 v5, 0x3f4c422a, v11
	v_add_f32_e32 v5, v5, v5
	v_mul_f32_e32 v5, 0xbfb8aa3b, v5
	v_exp_f32_e32 v5, v5
	s_nop 0
	v_add_f32_e32 v5, 1.0, v5
	v_rcp_f32_e32 v11, v5
	s_nop 0
	v_pk_mul_f32 v[8:9], v[10:11], v[8:9]
	s_nop 0
	v_pk_mul_f32 v[6:7], v[8:9], v[6:7]
	s_nop 0
	v_cvt_pk_bf16_f32 v5, v6, v7
	v_mad_i64_i32 v[6:7], s[4:5], v0, s13, v[72:73]
	global_store_dwordx4 v[6:7], v[2:5], off
	s_waitcnt lgkmcnt(0)
	s_cbranch_scc1 .LBB0_600
	v_readlane_b32 s44, v253, 43
	v_readlane_b32 s45, v253, 44
	s_movk_i32 s43, 0x4000
	v_readlane_b32 s47, v253, 50
